# speedup vs baseline: 1.0308x; 1.0108x over previous
_Z12k1_colsum_q8PKfPjPfS2_:
	s_load_dwordx8 s[4:11], s[0:1], 0x0
	v_and_b32_e32 v1, 63, v0
	v_lshrrev_b32_e32 v41, 6, v0
	s_mul_i32 s12, s2, 0xc35
	s_lshr_b32 s12, s12, 4
	v_readfirstlane_b32 s14, v41
	s_add_i32 s13, s2, 1
	s_mul_i32 s13, s13, 0xc35
	s_lshr_b32 s13, s13, 4
	s_sub_u32 s13, s13, s12
	s_sub_u32 s15, s13, 0xc0
	s_cmp_lt_u32 s14, s15
	s_cselect_b32 s29, 1, 0
	v_lshlrev_b32_e32 v34, 4, v1
	v_min_u32_e32 v35, 57, v1
	v_lshlrev_b32_e32 v35, 4, v35
	v_cmp_gt_u32_e64 s[18:19], 58, v1
	s_lshl_b32 s35, s14, 13
	s_add_u32 s36, s35, 0x1000
	v_add_u32_e32 v38, s35, v34
	v_lshrrev_b32_e32 v41, 5, v1
	v_mov_b32_e32 v42, 0xc35000
	v_mul_lo_u32 v39, v41, v42
	v_and_b32_e32 v42, 31, v1
	v_lshl_add_u32 v39, v42, 2, v39
	v_mov_b32_e32 v2, 0
	v_mov_b32_e32 v3, 0
	v_mov_b32_e32 v4, 0
	v_mov_b32_e32 v5, 0
	v_mov_b32_e32 v6, 0
	v_mov_b32_e32 v7, 0
	v_mov_b32_e32 v8, 0
	v_mov_b32_e32 v9, 0
	v_mov_b32_e32 v10, 0
	v_mov_b32_e32 v11, 0
	v_mov_b32_e32 v12, 0
	v_mov_b32_e32 v13, 0
	v_mov_b32_e32 v14, 0
	v_mov_b32_e32 v15, 0
	v_mov_b32_e32 v16, 0
	v_mov_b32_e32 v17, 0
	v_mov_b32_e32 v40, 0
	v_mov_b32_e32 v47, 0x42fe0000
	s_mov_b32 s32, 0x42fe0000
	s_mov_b32 s33, 0xc0c0400
	s_mov_b32 s34, 0x4000c0c
	s_add_u32 s15, s12, s14
	s_mul_i32 s37, s15, 0xfa0
	s_lshl_b32 s15, s15, 7
	s_waitcnt lgkmcnt(0)
	s_add_u32 s16, s4, s37
	s_addc_u32 s17, s5, 0
	s_add_u32 s40, s6, s15
	s_addc_u32 s41, s7, 0
	s_add_u32 s20, s40, 0
	s_addc_u32 s21, s41, 0
	s_add_u32 s22, s20, 0x186a000
	s_addc_u32 s23, s21, 0
	s_add_u32 s24, s22, 0x186a000
	s_addc_u32 s25, s23, 0
	s_add_u32 s26, s24, 0x186a000
	s_addc_u32 s27, s25, 0
	s_mov_b32 m0, s35
	s_nop 0
	global_load_lds_dwordx4 v34, s[16:17] nt
	global_load_lds_dwordx4 v34, s[16:17] offset:1024 nt
	global_load_lds_dwordx4 v34, s[16:17] offset:2048 nt
	global_load_lds_dwordx4 v35, s[16:17] offset:3072 nt
	s_add_u32 s16, s16, 0x7d00
	s_addc_u32 s17, s17, 0
	s_waitcnt vmcnt(0)
	ds_read_b128 v[18:21], v38 offset:0
	ds_read_b128 v[22:25], v38 offset:1024
	ds_read_b128 v[26:29], v38 offset:2048
	ds_read_b128 v[30:33], v38 offset:3072
	s_waitcnt lgkmcnt(0)
	s_barrier
	s_mov_b32 m0, s36
	s_nop 0
	global_load_lds_dwordx4 v34, s[16:17] nt
	global_load_lds_dwordx4 v34, s[16:17] offset:1024 nt
	global_load_lds_dwordx4 v34, s[16:17] offset:2048 nt
	global_load_lds_dwordx4 v35, s[16:17] offset:3072 nt
	s_add_u32 s16, s16, 0x7d00
	s_addc_u32 s17, s17, 0
	v_cndmask_b32_e64 v30, 0, v30, s[18:19]
	v_cndmask_b32_e64 v31, 0, v31, s[18:19]
	v_cndmask_b32_e64 v32, 0, v32, s[18:19]
	v_cndmask_b32_e64 v33, 0, v33, s[18:19]
	v_max3_f32 v41, |v18|, |v19|, |v20|
	v_max3_f32 v42, |v21|, |v22|, |v23|
	v_max3_f32 v43, |v24|, |v25|, |v26|
	v_max3_f32 v44, |v27|, |v28|, |v29|
	v_max3_f32 v48, |v30|, |v31|, |v32|
	v_max3_f32 v41, v41, v42, |v33|
	v_max3_f32 v43, v43, v44, v48
	v_max_f32_e32 v41, v41, v43
	v_pk_add_f32 v[2:3], v[2:3], v[18:19]
	v_pk_add_f32 v[4:5], v[4:5], v[20:21]
	v_max_f32_dpp v41, v41, v41 quad_perm:[1,0,3,2] row_mask:0xf bank_mask:0xf
	v_pk_add_f32 v[6:7], v[6:7], v[22:23]
	v_pk_add_f32 v[8:9], v[8:9], v[24:25]
	v_max_f32_dpp v41, v41, v41 quad_perm:[2,3,0,1] row_mask:0xf bank_mask:0xf
	v_pk_add_f32 v[10:11], v[10:11], v[26:27]
	v_pk_add_f32 v[12:13], v[12:13], v[28:29]
	v_max_f32_dpp v41, v41, v41 row_half_mirror row_mask:0xf bank_mask:0xf
	v_pk_add_f32 v[14:15], v[14:15], v[30:31]
	v_pk_add_f32 v[16:17], v[16:17], v[32:33]
	v_max_f32_dpp v41, v41, v41 row_mirror row_mask:0xf bank_mask:0xf
	s_nop 1
	v_max_f32_dpp v41, v41, v41 row_bcast:15 row_mask:0xa bank_mask:0xf
	s_nop 1
	v_max_f32_dpp v41, v41, v41 row_bcast:31 row_mask:0xc bank_mask:0xf
	s_nop 1
	v_readlane_b32 s28, v41, 63
	s_nop 1
	v_div_scale_f32 v48, s[30:31], s28, s28, v47
	v_rcp_f32_e32 v49, v48
	s_nop 0
	v_fma_f32 v50, -v48, v49, 1.0
	v_fmac_f32_e32 v49, v50, v49
	v_mov_b32_e32 v50, s28
	v_div_scale_f32 v50, vcc, s32, v50, s32
	v_mul_f32_e32 v51, v50, v49
	v_fma_f32 v52, -v48, v51, v50
	v_fmac_f32_e32 v51, v52, v49
	v_fma_f32 v48, -v48, v51, v50
	v_div_fmas_f32 v48, v48, v49, v51
	v_div_fixup_f32 v48, v48, s28, v47
	v_cmp_gt_f32_e64 vcc, s28, 0
	v_writelane_b32 v40, s28, 0
	s_nop 0
	v_cndmask_b32_e32 v48, 0, v48, vcc
	v_fmaak_f32 v49, v18, v48, 0x4b400000
	v_fmaak_f32 v50, v19, v48, 0x4b400000
	v_fmaak_f32 v51, v20, v48, 0x4b400000
	v_fmaak_f32 v52, v21, v48, 0x4b400000
	v_perm_b32 v49, v50, v49, s33
	v_perm_b32 v51, v52, v51, s34
	v_or_b32_e32 v56, v49, v51
	v_fmaak_f32 v41, v22, v48, 0x4b400000
	v_fmaak_f32 v42, v23, v48, 0x4b400000
	v_fmaak_f32 v43, v24, v48, 0x4b400000
	v_fmaak_f32 v44, v25, v48, 0x4b400000
	v_perm_b32 v41, v42, v41, s33
	v_perm_b32 v43, v44, v43, s34
	v_or_b32_e32 v57, v41, v43
	v_fmaak_f32 v49, v26, v48, 0x4b400000
	v_fmaak_f32 v50, v27, v48, 0x4b400000
	v_fmaak_f32 v51, v28, v48, 0x4b400000
	v_fmaak_f32 v52, v29, v48, 0x4b400000
	v_perm_b32 v49, v50, v49, s33
	v_perm_b32 v51, v52, v51, s34
	v_or_b32_e32 v58, v49, v51
	v_fmaak_f32 v41, v30, v48, 0x4b400000
	v_fmaak_f32 v42, v31, v48, 0x4b400000
	v_fmaak_f32 v43, v32, v48, 0x4b400000
	v_fmaak_f32 v44, v33, v48, 0x4b400000
	v_perm_b32 v41, v42, v41, s33
	v_perm_b32 v43, v44, v43, s34
	v_or_b32_e32 v59, v41, v43
	s_waitcnt vmcnt(0)
	ds_read_b128 v[18:21], v38 offset:4096
	ds_read_b128 v[22:25], v38 offset:5120
	ds_read_b128 v[26:29], v38 offset:6144
	ds_read_b128 v[30:33], v38 offset:7168
	s_waitcnt lgkmcnt(0)
	s_barrier
	s_mov_b32 m0, s35
	s_nop 0
	global_load_lds_dwordx4 v34, s[16:17] nt
	global_load_lds_dwordx4 v34, s[16:17] offset:1024 nt
	global_load_lds_dwordx4 v34, s[16:17] offset:2048 nt
	global_load_lds_dwordx4 v35, s[16:17] offset:3072 nt
	s_add_u32 s16, s16, 0x7d00
	s_addc_u32 s17, s17, 0
	v_cndmask_b32_e64 v30, 0, v30, s[18:19]
	v_cndmask_b32_e64 v31, 0, v31, s[18:19]
	v_cndmask_b32_e64 v32, 0, v32, s[18:19]
	v_cndmask_b32_e64 v33, 0, v33, s[18:19]
	v_max3_f32 v41, |v18|, |v19|, |v20|
	v_max3_f32 v42, |v21|, |v22|, |v23|
	v_max3_f32 v43, |v24|, |v25|, |v26|
	v_max3_f32 v44, |v27|, |v28|, |v29|
	v_max3_f32 v48, |v30|, |v31|, |v32|
	v_max3_f32 v41, v41, v42, |v33|
	v_max3_f32 v43, v43, v44, v48
	v_max_f32_e32 v41, v41, v43
	v_pk_add_f32 v[2:3], v[2:3], v[18:19]
	v_pk_add_f32 v[4:5], v[4:5], v[20:21]
	v_max_f32_dpp v41, v41, v41 quad_perm:[1,0,3,2] row_mask:0xf bank_mask:0xf
	v_pk_add_f32 v[6:7], v[6:7], v[22:23]
	v_pk_add_f32 v[8:9], v[8:9], v[24:25]
	v_max_f32_dpp v41, v41, v41 quad_perm:[2,3,0,1] row_mask:0xf bank_mask:0xf
	v_pk_add_f32 v[10:11], v[10:11], v[26:27]
	v_pk_add_f32 v[12:13], v[12:13], v[28:29]
	v_max_f32_dpp v41, v41, v41 row_half_mirror row_mask:0xf bank_mask:0xf
	v_pk_add_f32 v[14:15], v[14:15], v[30:31]
	v_pk_add_f32 v[16:17], v[16:17], v[32:33]
	v_max_f32_dpp v41, v41, v41 row_mirror row_mask:0xf bank_mask:0xf
	s_nop 1
	v_max_f32_dpp v41, v41, v41 row_bcast:15 row_mask:0xa bank_mask:0xf
	s_nop 1
	v_max_f32_dpp v41, v41, v41 row_bcast:31 row_mask:0xc bank_mask:0xf
	s_nop 1
	v_readlane_b32 s28, v41, 63
	s_nop 1
	v_div_scale_f32 v48, s[30:31], s28, s28, v47
	v_rcp_f32_e32 v49, v48
	s_nop 0
	v_fma_f32 v50, -v48, v49, 1.0
	v_fmac_f32_e32 v49, v50, v49
	v_mov_b32_e32 v50, s28
	v_div_scale_f32 v50, vcc, s32, v50, s32
	v_mul_f32_e32 v51, v50, v49
	v_fma_f32 v52, -v48, v51, v50
	v_fmac_f32_e32 v51, v52, v49
	v_fma_f32 v48, -v48, v51, v50
	v_div_fmas_f32 v48, v48, v49, v51
	v_div_fixup_f32 v48, v48, s28, v47
	v_cmp_gt_f32_e64 vcc, s28, 0
	v_writelane_b32 v40, s28, 1
	s_nop 0
	v_cndmask_b32_e32 v48, 0, v48, vcc
	v_fmaak_f32 v49, v18, v48, 0x4b400000
	v_fmaak_f32 v50, v19, v48, 0x4b400000
	v_fmaak_f32 v51, v20, v48, 0x4b400000
	v_fmaak_f32 v52, v21, v48, 0x4b400000
	v_perm_b32 v49, v50, v49, s33
	v_perm_b32 v51, v52, v51, s34
	v_or_b32_e32 v60, v49, v51
	v_fmaak_f32 v41, v22, v48, 0x4b400000
	v_fmaak_f32 v42, v23, v48, 0x4b400000
	v_fmaak_f32 v43, v24, v48, 0x4b400000
	v_fmaak_f32 v44, v25, v48, 0x4b400000
	v_perm_b32 v41, v42, v41, s33
	v_perm_b32 v43, v44, v43, s34
	v_or_b32_e32 v61, v41, v43
	v_fmaak_f32 v49, v26, v48, 0x4b400000
	v_fmaak_f32 v50, v27, v48, 0x4b400000
	v_fmaak_f32 v51, v28, v48, 0x4b400000
	v_fmaak_f32 v52, v29, v48, 0x4b400000
	v_perm_b32 v49, v50, v49, s33
	v_perm_b32 v51, v52, v51, s34
	v_or_b32_e32 v62, v49, v51
	v_fmaak_f32 v41, v30, v48, 0x4b400000
	v_fmaak_f32 v42, v31, v48, 0x4b400000
	v_fmaak_f32 v43, v32, v48, 0x4b400000
	v_fmaak_f32 v44, v33, v48, 0x4b400000
	v_perm_b32 v41, v42, v41, s33
	v_perm_b32 v43, v44, v43, s34
	v_or_b32_e32 v63, v41, v43
	s_waitcnt vmcnt(0)
	ds_read_b128 v[18:21], v38 offset:0
	ds_read_b128 v[22:25], v38 offset:1024
	ds_read_b128 v[26:29], v38 offset:2048
	ds_read_b128 v[30:33], v38 offset:3072
	s_waitcnt lgkmcnt(0)
	s_barrier
	s_mov_b32 m0, s36
	s_nop 0
	global_load_lds_dwordx4 v34, s[16:17] nt
	global_load_lds_dwordx4 v34, s[16:17] offset:1024 nt
	global_load_lds_dwordx4 v34, s[16:17] offset:2048 nt
	global_load_lds_dwordx4 v35, s[16:17] offset:3072 nt
	s_add_u32 s16, s16, 0x7d00
	s_addc_u32 s17, s17, 0
	v_cndmask_b32_e64 v30, 0, v30, s[18:19]
	v_cndmask_b32_e64 v31, 0, v31, s[18:19]
	v_cndmask_b32_e64 v32, 0, v32, s[18:19]
	v_cndmask_b32_e64 v33, 0, v33, s[18:19]
	v_max3_f32 v41, |v18|, |v19|, |v20|
	v_max3_f32 v42, |v21|, |v22|, |v23|
	v_max3_f32 v43, |v24|, |v25|, |v26|
	v_max3_f32 v44, |v27|, |v28|, |v29|
	v_max3_f32 v48, |v30|, |v31|, |v32|
	v_max3_f32 v41, v41, v42, |v33|
	v_max3_f32 v43, v43, v44, v48
	v_max_f32_e32 v41, v41, v43
	v_pk_add_f32 v[2:3], v[2:3], v[18:19]
	v_pk_add_f32 v[4:5], v[4:5], v[20:21]
	v_max_f32_dpp v41, v41, v41 quad_perm:[1,0,3,2] row_mask:0xf bank_mask:0xf
	v_pk_add_f32 v[6:7], v[6:7], v[22:23]
	v_pk_add_f32 v[8:9], v[8:9], v[24:25]
	v_max_f32_dpp v41, v41, v41 quad_perm:[2,3,0,1] row_mask:0xf bank_mask:0xf
	v_pk_add_f32 v[10:11], v[10:11], v[26:27]
	v_pk_add_f32 v[12:13], v[12:13], v[28:29]
	v_max_f32_dpp v41, v41, v41 row_half_mirror row_mask:0xf bank_mask:0xf
	v_pk_add_f32 v[14:15], v[14:15], v[30:31]
	v_pk_add_f32 v[16:17], v[16:17], v[32:33]
	v_max_f32_dpp v41, v41, v41 row_mirror row_mask:0xf bank_mask:0xf
	s_nop 1
	v_max_f32_dpp v41, v41, v41 row_bcast:15 row_mask:0xa bank_mask:0xf
	s_nop 1
	v_max_f32_dpp v41, v41, v41 row_bcast:31 row_mask:0xc bank_mask:0xf
	s_nop 1
	v_readlane_b32 s28, v41, 63
	s_nop 1
	v_div_scale_f32 v48, s[30:31], s28, s28, v47
	v_rcp_f32_e32 v49, v48
	s_nop 0
	v_fma_f32 v50, -v48, v49, 1.0
	v_fmac_f32_e32 v49, v50, v49
	v_mov_b32_e32 v50, s28
	v_div_scale_f32 v50, vcc, s32, v50, s32
	v_mul_f32_e32 v51, v50, v49
	v_fma_f32 v52, -v48, v51, v50
	v_fmac_f32_e32 v51, v52, v49
	v_fma_f32 v48, -v48, v51, v50
	v_div_fmas_f32 v48, v48, v49, v51
	v_div_fixup_f32 v48, v48, s28, v47
	v_cmp_gt_f32_e64 vcc, s28, 0
	v_writelane_b32 v40, s28, 2
	s_nop 0
	v_cndmask_b32_e32 v48, 0, v48, vcc
	v_fmaak_f32 v49, v18, v48, 0x4b400000
	v_fmaak_f32 v50, v19, v48, 0x4b400000
	v_fmaak_f32 v51, v20, v48, 0x4b400000
	v_fmaak_f32 v52, v21, v48, 0x4b400000
	v_perm_b32 v49, v50, v49, s33
	v_perm_b32 v51, v52, v51, s34
	v_or_b32_e32 v64, v49, v51
	v_fmaak_f32 v41, v22, v48, 0x4b400000
	v_fmaak_f32 v42, v23, v48, 0x4b400000
	v_fmaak_f32 v43, v24, v48, 0x4b400000
	v_fmaak_f32 v44, v25, v48, 0x4b400000
	v_perm_b32 v41, v42, v41, s33
	v_perm_b32 v43, v44, v43, s34
	v_or_b32_e32 v65, v41, v43
	v_fmaak_f32 v49, v26, v48, 0x4b400000
	v_fmaak_f32 v50, v27, v48, 0x4b400000
	v_fmaak_f32 v51, v28, v48, 0x4b400000
	v_fmaak_f32 v52, v29, v48, 0x4b400000
	v_perm_b32 v49, v50, v49, s33
	v_perm_b32 v51, v52, v51, s34
	v_or_b32_e32 v66, v49, v51
	v_fmaak_f32 v41, v30, v48, 0x4b400000
	v_fmaak_f32 v42, v31, v48, 0x4b400000
	v_fmaak_f32 v43, v32, v48, 0x4b400000
	v_fmaak_f32 v44, v33, v48, 0x4b400000
	v_perm_b32 v41, v42, v41, s33
	v_perm_b32 v43, v44, v43, s34
	v_or_b32_e32 v67, v41, v43
	s_waitcnt vmcnt(0)
	ds_read_b128 v[18:21], v38 offset:4096
	ds_read_b128 v[22:25], v38 offset:5120
	ds_read_b128 v[26:29], v38 offset:6144
	ds_read_b128 v[30:33], v38 offset:7168
	s_waitcnt lgkmcnt(0)
	s_barrier
	s_mov_b32 m0, s35
	s_nop 0
	global_load_lds_dwordx4 v34, s[16:17] nt
	global_load_lds_dwordx4 v34, s[16:17] offset:1024 nt
	global_load_lds_dwordx4 v34, s[16:17] offset:2048 nt
	global_load_lds_dwordx4 v35, s[16:17] offset:3072 nt
	s_add_u32 s16, s16, 0x7d00
	s_addc_u32 s17, s17, 0
	v_cndmask_b32_e64 v30, 0, v30, s[18:19]
	v_cndmask_b32_e64 v31, 0, v31, s[18:19]
	v_cndmask_b32_e64 v32, 0, v32, s[18:19]
	v_cndmask_b32_e64 v33, 0, v33, s[18:19]
	v_max3_f32 v41, |v18|, |v19|, |v20|
	v_max3_f32 v42, |v21|, |v22|, |v23|
	v_max3_f32 v43, |v24|, |v25|, |v26|
	v_max3_f32 v44, |v27|, |v28|, |v29|
	v_max3_f32 v48, |v30|, |v31|, |v32|
	v_max3_f32 v41, v41, v42, |v33|
	v_max3_f32 v43, v43, v44, v48
	v_max_f32_e32 v41, v41, v43
	v_pk_add_f32 v[2:3], v[2:3], v[18:19]
	v_pk_add_f32 v[4:5], v[4:5], v[20:21]
	v_max_f32_dpp v41, v41, v41 quad_perm:[1,0,3,2] row_mask:0xf bank_mask:0xf
	v_pk_add_f32 v[6:7], v[6:7], v[22:23]
	v_pk_add_f32 v[8:9], v[8:9], v[24:25]
	v_max_f32_dpp v41, v41, v41 quad_perm:[2,3,0,1] row_mask:0xf bank_mask:0xf
	v_pk_add_f32 v[10:11], v[10:11], v[26:27]
	v_pk_add_f32 v[12:13], v[12:13], v[28:29]
	v_max_f32_dpp v41, v41, v41 row_half_mirror row_mask:0xf bank_mask:0xf
	v_pk_add_f32 v[14:15], v[14:15], v[30:31]
	v_pk_add_f32 v[16:17], v[16:17], v[32:33]
	v_max_f32_dpp v41, v41, v41 row_mirror row_mask:0xf bank_mask:0xf
	s_nop 1
	v_max_f32_dpp v41, v41, v41 row_bcast:15 row_mask:0xa bank_mask:0xf
	s_nop 1
	v_max_f32_dpp v41, v41, v41 row_bcast:31 row_mask:0xc bank_mask:0xf
	s_nop 1
	v_readlane_b32 s28, v41, 63
	s_nop 1
	v_div_scale_f32 v48, s[30:31], s28, s28, v47
	v_rcp_f32_e32 v49, v48
	s_nop 0
	v_fma_f32 v50, -v48, v49, 1.0
	v_fmac_f32_e32 v49, v50, v49
	v_mov_b32_e32 v50, s28
	v_div_scale_f32 v50, vcc, s32, v50, s32
	v_mul_f32_e32 v51, v50, v49
	v_fma_f32 v52, -v48, v51, v50
	v_fmac_f32_e32 v51, v52, v49
	v_fma_f32 v48, -v48, v51, v50
	v_div_fmas_f32 v48, v48, v49, v51
	v_div_fixup_f32 v48, v48, s28, v47
	v_cmp_gt_f32_e64 vcc, s28, 0
	v_writelane_b32 v40, s28, 3
	s_nop 0
	v_cndmask_b32_e32 v48, 0, v48, vcc
	v_fmaak_f32 v49, v18, v48, 0x4b400000
	v_fmaak_f32 v50, v19, v48, 0x4b400000
	v_fmaak_f32 v51, v20, v48, 0x4b400000
	v_fmaak_f32 v52, v21, v48, 0x4b400000
	v_perm_b32 v49, v50, v49, s33
	v_perm_b32 v51, v52, v51, s34
	v_or_b32_e32 v68, v49, v51
	v_fmaak_f32 v41, v22, v48, 0x4b400000
	v_fmaak_f32 v42, v23, v48, 0x4b400000
	v_fmaak_f32 v43, v24, v48, 0x4b400000
	v_fmaak_f32 v44, v25, v48, 0x4b400000
	v_perm_b32 v41, v42, v41, s33
	v_perm_b32 v43, v44, v43, s34
	v_or_b32_e32 v69, v41, v43
	v_fmaak_f32 v49, v26, v48, 0x4b400000
	v_fmaak_f32 v50, v27, v48, 0x4b400000
	v_fmaak_f32 v51, v28, v48, 0x4b400000
	v_fmaak_f32 v52, v29, v48, 0x4b400000
	v_perm_b32 v49, v50, v49, s33
	v_perm_b32 v51, v52, v51, s34
	v_or_b32_e32 v70, v49, v51
	v_fmaak_f32 v41, v30, v48, 0x4b400000
	v_fmaak_f32 v42, v31, v48, 0x4b400000
	v_fmaak_f32 v43, v32, v48, 0x4b400000
	v_fmaak_f32 v44, v33, v48, 0x4b400000
	v_perm_b32 v41, v42, v41, s33
	v_perm_b32 v43, v44, v43, s34
	v_or_b32_e32 v71, v41, v43
	s_waitcnt vmcnt(0)
	ds_read_b128 v[18:21], v38 offset:0
	ds_read_b128 v[22:25], v38 offset:1024
	ds_read_b128 v[26:29], v38 offset:2048
	ds_read_b128 v[30:33], v38 offset:3072
	s_waitcnt lgkmcnt(0)
	s_barrier
	s_mov_b32 m0, s36
	s_nop 0
	global_load_lds_dwordx4 v34, s[16:17] nt
	global_load_lds_dwordx4 v34, s[16:17] offset:1024 nt
	global_load_lds_dwordx4 v34, s[16:17] offset:2048 nt
	global_load_lds_dwordx4 v35, s[16:17] offset:3072 nt
	s_add_u32 s16, s16, 0x7d00
	s_addc_u32 s17, s17, 0
	v_cndmask_b32_e64 v30, 0, v30, s[18:19]
	v_cndmask_b32_e64 v31, 0, v31, s[18:19]
	v_cndmask_b32_e64 v32, 0, v32, s[18:19]
	v_cndmask_b32_e64 v33, 0, v33, s[18:19]
	v_max3_f32 v41, |v18|, |v19|, |v20|
	v_max3_f32 v42, |v21|, |v22|, |v23|
	v_max3_f32 v43, |v24|, |v25|, |v26|
	v_max3_f32 v44, |v27|, |v28|, |v29|
	v_max3_f32 v48, |v30|, |v31|, |v32|
	v_max3_f32 v41, v41, v42, |v33|
	v_max3_f32 v43, v43, v44, v48
	v_max_f32_e32 v41, v41, v43
	v_pk_add_f32 v[2:3], v[2:3], v[18:19]
	v_pk_add_f32 v[4:5], v[4:5], v[20:21]
	v_max_f32_dpp v41, v41, v41 quad_perm:[1,0,3,2] row_mask:0xf bank_mask:0xf
	v_pk_add_f32 v[6:7], v[6:7], v[22:23]
	v_pk_add_f32 v[8:9], v[8:9], v[24:25]
	v_max_f32_dpp v41, v41, v41 quad_perm:[2,3,0,1] row_mask:0xf bank_mask:0xf
	v_pk_add_f32 v[10:11], v[10:11], v[26:27]
	v_pk_add_f32 v[12:13], v[12:13], v[28:29]
	v_max_f32_dpp v41, v41, v41 row_half_mirror row_mask:0xf bank_mask:0xf
	v_pk_add_f32 v[14:15], v[14:15], v[30:31]
	v_pk_add_f32 v[16:17], v[16:17], v[32:33]
	v_max_f32_dpp v41, v41, v41 row_mirror row_mask:0xf bank_mask:0xf
	s_nop 1
	v_max_f32_dpp v41, v41, v41 row_bcast:15 row_mask:0xa bank_mask:0xf
	s_nop 1
	v_max_f32_dpp v41, v41, v41 row_bcast:31 row_mask:0xc bank_mask:0xf
	s_nop 1
	v_readlane_b32 s28, v41, 63
	s_nop 1
	v_div_scale_f32 v48, s[30:31], s28, s28, v47
	v_rcp_f32_e32 v49, v48
	s_nop 0
	v_fma_f32 v50, -v48, v49, 1.0
	v_fmac_f32_e32 v49, v50, v49
	v_mov_b32_e32 v50, s28
	v_div_scale_f32 v50, vcc, s32, v50, s32
	v_mul_f32_e32 v51, v50, v49
	v_fma_f32 v52, -v48, v51, v50
	v_fmac_f32_e32 v51, v52, v49
	v_fma_f32 v48, -v48, v51, v50
	v_div_fmas_f32 v48, v48, v49, v51
	v_div_fixup_f32 v48, v48, s28, v47
	v_cmp_gt_f32_e64 vcc, s28, 0
	v_writelane_b32 v40, s28, 4
	s_nop 0
	v_cndmask_b32_e32 v48, 0, v48, vcc
	v_fmaak_f32 v49, v18, v48, 0x4b400000
	v_fmaak_f32 v50, v19, v48, 0x4b400000
	v_fmaak_f32 v51, v20, v48, 0x4b400000
	v_fmaak_f32 v52, v21, v48, 0x4b400000
	v_perm_b32 v49, v50, v49, s33
	v_perm_b32 v51, v52, v51, s34
	v_or_b32_e32 v72, v49, v51
	v_fmaak_f32 v41, v22, v48, 0x4b400000
	v_fmaak_f32 v42, v23, v48, 0x4b400000
	v_fmaak_f32 v43, v24, v48, 0x4b400000
	v_fmaak_f32 v44, v25, v48, 0x4b400000
	v_perm_b32 v41, v42, v41, s33
	v_perm_b32 v43, v44, v43, s34
	v_or_b32_e32 v73, v41, v43
	v_fmaak_f32 v49, v26, v48, 0x4b400000
	v_fmaak_f32 v50, v27, v48, 0x4b400000
	v_fmaak_f32 v51, v28, v48, 0x4b400000
	v_fmaak_f32 v52, v29, v48, 0x4b400000
	v_perm_b32 v49, v50, v49, s33
	v_perm_b32 v51, v52, v51, s34
	v_or_b32_e32 v74, v49, v51
	v_fmaak_f32 v41, v30, v48, 0x4b400000
	v_fmaak_f32 v42, v31, v48, 0x4b400000
	v_fmaak_f32 v43, v32, v48, 0x4b400000
	v_fmaak_f32 v44, v33, v48, 0x4b400000
	v_perm_b32 v41, v42, v41, s33
	v_perm_b32 v43, v44, v43, s34
	v_or_b32_e32 v75, v41, v43
	s_waitcnt vmcnt(0)
	ds_read_b128 v[18:21], v38 offset:4096
	ds_read_b128 v[22:25], v38 offset:5120
	ds_read_b128 v[26:29], v38 offset:6144
	ds_read_b128 v[30:33], v38 offset:7168
	s_waitcnt lgkmcnt(0)
	s_barrier
	s_mov_b32 m0, s35
	s_nop 0
	global_load_lds_dwordx4 v34, s[16:17] nt
	global_load_lds_dwordx4 v34, s[16:17] offset:1024 nt
	global_load_lds_dwordx4 v34, s[16:17] offset:2048 nt
	global_load_lds_dwordx4 v35, s[16:17] offset:3072 nt
	s_add_u32 s16, s16, 0x7d00
	s_addc_u32 s17, s17, 0
	v_cndmask_b32_e64 v30, 0, v30, s[18:19]
	v_cndmask_b32_e64 v31, 0, v31, s[18:19]
	v_cndmask_b32_e64 v32, 0, v32, s[18:19]
	v_cndmask_b32_e64 v33, 0, v33, s[18:19]
	v_max3_f32 v41, |v18|, |v19|, |v20|
	v_max3_f32 v42, |v21|, |v22|, |v23|
	v_max3_f32 v43, |v24|, |v25|, |v26|
	v_max3_f32 v44, |v27|, |v28|, |v29|
	v_max3_f32 v48, |v30|, |v31|, |v32|
	v_max3_f32 v41, v41, v42, |v33|
	v_max3_f32 v43, v43, v44, v48
	v_max_f32_e32 v41, v41, v43
	v_pk_add_f32 v[2:3], v[2:3], v[18:19]
	v_pk_add_f32 v[4:5], v[4:5], v[20:21]
	v_max_f32_dpp v41, v41, v41 quad_perm:[1,0,3,2] row_mask:0xf bank_mask:0xf
	v_pk_add_f32 v[6:7], v[6:7], v[22:23]
	v_pk_add_f32 v[8:9], v[8:9], v[24:25]
	v_max_f32_dpp v41, v41, v41 quad_perm:[2,3,0,1] row_mask:0xf bank_mask:0xf
	v_pk_add_f32 v[10:11], v[10:11], v[26:27]
	v_pk_add_f32 v[12:13], v[12:13], v[28:29]
	v_max_f32_dpp v41, v41, v41 row_half_mirror row_mask:0xf bank_mask:0xf
	v_pk_add_f32 v[14:15], v[14:15], v[30:31]
	v_pk_add_f32 v[16:17], v[16:17], v[32:33]
	v_max_f32_dpp v41, v41, v41 row_mirror row_mask:0xf bank_mask:0xf
	s_nop 1
	v_max_f32_dpp v41, v41, v41 row_bcast:15 row_mask:0xa bank_mask:0xf
	s_nop 1
	v_max_f32_dpp v41, v41, v41 row_bcast:31 row_mask:0xc bank_mask:0xf
	s_nop 1
	v_readlane_b32 s28, v41, 63
	s_nop 1
	v_div_scale_f32 v48, s[30:31], s28, s28, v47
	v_rcp_f32_e32 v49, v48
	s_nop 0
	v_fma_f32 v50, -v48, v49, 1.0
	v_fmac_f32_e32 v49, v50, v49
	v_mov_b32_e32 v50, s28
	v_div_scale_f32 v50, vcc, s32, v50, s32
	v_mul_f32_e32 v51, v50, v49
	v_fma_f32 v52, -v48, v51, v50
	v_fmac_f32_e32 v51, v52, v49
	v_fma_f32 v48, -v48, v51, v50
	v_div_fmas_f32 v48, v48, v49, v51
	v_div_fixup_f32 v48, v48, s28, v47
	v_cmp_gt_f32_e64 vcc, s28, 0
	v_writelane_b32 v40, s28, 5
	s_nop 0
	v_cndmask_b32_e32 v48, 0, v48, vcc
	v_fmaak_f32 v49, v18, v48, 0x4b400000
	v_fmaak_f32 v50, v19, v48, 0x4b400000
	v_fmaak_f32 v51, v20, v48, 0x4b400000
	v_fmaak_f32 v52, v21, v48, 0x4b400000
	v_perm_b32 v49, v50, v49, s33
	v_perm_b32 v51, v52, v51, s34
	v_or_b32_e32 v76, v49, v51
	v_fmaak_f32 v41, v22, v48, 0x4b400000
	v_fmaak_f32 v42, v23, v48, 0x4b400000
	v_fmaak_f32 v43, v24, v48, 0x4b400000
	v_fmaak_f32 v44, v25, v48, 0x4b400000
	v_perm_b32 v41, v42, v41, s33
	v_perm_b32 v43, v44, v43, s34
	v_or_b32_e32 v77, v41, v43
	v_fmaak_f32 v49, v26, v48, 0x4b400000
	v_fmaak_f32 v50, v27, v48, 0x4b400000
	v_fmaak_f32 v51, v28, v48, 0x4b400000
	v_fmaak_f32 v52, v29, v48, 0x4b400000
	v_perm_b32 v49, v50, v49, s33
	v_perm_b32 v51, v52, v51, s34
	v_or_b32_e32 v78, v49, v51
	v_fmaak_f32 v41, v30, v48, 0x4b400000
	v_fmaak_f32 v42, v31, v48, 0x4b400000
	v_fmaak_f32 v43, v32, v48, 0x4b400000
	v_fmaak_f32 v44, v33, v48, 0x4b400000
	v_perm_b32 v41, v42, v41, s33
	v_perm_b32 v43, v44, v43, s34
	v_or_b32_e32 v79, v41, v43
	s_waitcnt vmcnt(0)
	ds_read_b128 v[18:21], v38 offset:0
	ds_read_b128 v[22:25], v38 offset:1024
	ds_read_b128 v[26:29], v38 offset:2048
	ds_read_b128 v[30:33], v38 offset:3072
	s_waitcnt lgkmcnt(0)
	s_barrier
	s_mov_b32 m0, s36
	s_nop 0
	global_load_lds_dwordx4 v34, s[16:17] nt
	global_load_lds_dwordx4 v34, s[16:17] offset:1024 nt
	global_load_lds_dwordx4 v34, s[16:17] offset:2048 nt
	global_load_lds_dwordx4 v35, s[16:17] offset:3072 nt
	s_add_u32 s16, s16, 0x7d00
	s_addc_u32 s17, s17, 0
	v_cndmask_b32_e64 v30, 0, v30, s[18:19]
	v_cndmask_b32_e64 v31, 0, v31, s[18:19]
	v_cndmask_b32_e64 v32, 0, v32, s[18:19]
	v_cndmask_b32_e64 v33, 0, v33, s[18:19]
	v_max3_f32 v41, |v18|, |v19|, |v20|
	v_max3_f32 v42, |v21|, |v22|, |v23|
	v_max3_f32 v43, |v24|, |v25|, |v26|
	v_max3_f32 v44, |v27|, |v28|, |v29|
	v_max3_f32 v48, |v30|, |v31|, |v32|
	v_max3_f32 v41, v41, v42, |v33|
	v_max3_f32 v43, v43, v44, v48
	v_max_f32_e32 v41, v41, v43
	v_pk_add_f32 v[2:3], v[2:3], v[18:19]
	v_pk_add_f32 v[4:5], v[4:5], v[20:21]
	v_max_f32_dpp v41, v41, v41 quad_perm:[1,0,3,2] row_mask:0xf bank_mask:0xf
	v_pk_add_f32 v[6:7], v[6:7], v[22:23]
	v_pk_add_f32 v[8:9], v[8:9], v[24:25]
	v_max_f32_dpp v41, v41, v41 quad_perm:[2,3,0,1] row_mask:0xf bank_mask:0xf
	v_pk_add_f32 v[10:11], v[10:11], v[26:27]
	v_pk_add_f32 v[12:13], v[12:13], v[28:29]
	v_max_f32_dpp v41, v41, v41 row_half_mirror row_mask:0xf bank_mask:0xf
	v_pk_add_f32 v[14:15], v[14:15], v[30:31]
	v_pk_add_f32 v[16:17], v[16:17], v[32:33]
	v_max_f32_dpp v41, v41, v41 row_mirror row_mask:0xf bank_mask:0xf
	s_nop 1
	v_max_f32_dpp v41, v41, v41 row_bcast:15 row_mask:0xa bank_mask:0xf
	s_nop 1
	v_max_f32_dpp v41, v41, v41 row_bcast:31 row_mask:0xc bank_mask:0xf
	s_nop 1
	v_readlane_b32 s28, v41, 63
	s_nop 1
	v_div_scale_f32 v48, s[30:31], s28, s28, v47
	v_rcp_f32_e32 v49, v48
	s_nop 0
	v_fma_f32 v50, -v48, v49, 1.0
	v_fmac_f32_e32 v49, v50, v49
	v_mov_b32_e32 v50, s28
	v_div_scale_f32 v50, vcc, s32, v50, s32
	v_mul_f32_e32 v51, v50, v49
	v_fma_f32 v52, -v48, v51, v50
	v_fmac_f32_e32 v51, v52, v49
	v_fma_f32 v48, -v48, v51, v50
	v_div_fmas_f32 v48, v48, v49, v51
	v_div_fixup_f32 v48, v48, s28, v47
	v_cmp_gt_f32_e64 vcc, s28, 0
	v_writelane_b32 v40, s28, 6
	s_nop 0
	v_cndmask_b32_e32 v48, 0, v48, vcc
	v_fmaak_f32 v49, v18, v48, 0x4b400000
	v_fmaak_f32 v50, v19, v48, 0x4b400000
	v_fmaak_f32 v51, v20, v48, 0x4b400000
	v_fmaak_f32 v52, v21, v48, 0x4b400000
	v_perm_b32 v49, v50, v49, s33
	v_perm_b32 v51, v52, v51, s34
	v_or_b32_e32 v80, v49, v51
	v_fmaak_f32 v41, v22, v48, 0x4b400000
	v_fmaak_f32 v42, v23, v48, 0x4b400000
	v_fmaak_f32 v43, v24, v48, 0x4b400000
	v_fmaak_f32 v44, v25, v48, 0x4b400000
	v_perm_b32 v41, v42, v41, s33
	v_perm_b32 v43, v44, v43, s34
	v_or_b32_e32 v81, v41, v43
	v_fmaak_f32 v49, v26, v48, 0x4b400000
	v_fmaak_f32 v50, v27, v48, 0x4b400000
	v_fmaak_f32 v51, v28, v48, 0x4b400000
	v_fmaak_f32 v52, v29, v48, 0x4b400000
	v_perm_b32 v49, v50, v49, s33
	v_perm_b32 v51, v52, v51, s34
	v_or_b32_e32 v82, v49, v51
	v_fmaak_f32 v41, v30, v48, 0x4b400000
	v_fmaak_f32 v42, v31, v48, 0x4b400000
	v_fmaak_f32 v43, v32, v48, 0x4b400000
	v_fmaak_f32 v44, v33, v48, 0x4b400000
	v_perm_b32 v41, v42, v41, s33
	v_perm_b32 v43, v44, v43, s34
	v_or_b32_e32 v83, v41, v43
	s_waitcnt vmcnt(0)
	ds_read_b128 v[18:21], v38 offset:4096
	ds_read_b128 v[22:25], v38 offset:5120
	ds_read_b128 v[26:29], v38 offset:6144
	ds_read_b128 v[30:33], v38 offset:7168
	s_waitcnt lgkmcnt(0)
	s_barrier
	s_mov_b32 m0, s35
	s_nop 0
	global_load_lds_dwordx4 v34, s[16:17] nt
	global_load_lds_dwordx4 v34, s[16:17] offset:1024 nt
	global_load_lds_dwordx4 v34, s[16:17] offset:2048 nt
	global_load_lds_dwordx4 v35, s[16:17] offset:3072 nt
	s_add_u32 s16, s16, 0x7d00
	s_addc_u32 s17, s17, 0
	v_cndmask_b32_e64 v30, 0, v30, s[18:19]
	v_cndmask_b32_e64 v31, 0, v31, s[18:19]
	v_cndmask_b32_e64 v32, 0, v32, s[18:19]
	v_cndmask_b32_e64 v33, 0, v33, s[18:19]
	v_max3_f32 v41, |v18|, |v19|, |v20|
	v_max3_f32 v42, |v21|, |v22|, |v23|
	v_max3_f32 v43, |v24|, |v25|, |v26|
	v_max3_f32 v44, |v27|, |v28|, |v29|
	v_max3_f32 v48, |v30|, |v31|, |v32|
	v_max3_f32 v41, v41, v42, |v33|
	v_max3_f32 v43, v43, v44, v48
	v_max_f32_e32 v41, v41, v43
	v_pk_add_f32 v[2:3], v[2:3], v[18:19]
	v_pk_add_f32 v[4:5], v[4:5], v[20:21]
	v_max_f32_dpp v41, v41, v41 quad_perm:[1,0,3,2] row_mask:0xf bank_mask:0xf
	v_pk_add_f32 v[6:7], v[6:7], v[22:23]
	v_pk_add_f32 v[8:9], v[8:9], v[24:25]
	v_max_f32_dpp v41, v41, v41 quad_perm:[2,3,0,1] row_mask:0xf bank_mask:0xf
	v_pk_add_f32 v[10:11], v[10:11], v[26:27]
	v_pk_add_f32 v[12:13], v[12:13], v[28:29]
	v_max_f32_dpp v41, v41, v41 row_half_mirror row_mask:0xf bank_mask:0xf
	v_pk_add_f32 v[14:15], v[14:15], v[30:31]
	v_pk_add_f32 v[16:17], v[16:17], v[32:33]
	v_max_f32_dpp v41, v41, v41 row_mirror row_mask:0xf bank_mask:0xf
	s_nop 1
	v_max_f32_dpp v41, v41, v41 row_bcast:15 row_mask:0xa bank_mask:0xf
	s_nop 1
	v_max_f32_dpp v41, v41, v41 row_bcast:31 row_mask:0xc bank_mask:0xf
	s_nop 1
	v_readlane_b32 s28, v41, 63
	s_nop 1
	v_div_scale_f32 v48, s[30:31], s28, s28, v47
	v_rcp_f32_e32 v49, v48
	s_nop 0
	v_fma_f32 v50, -v48, v49, 1.0
	v_fmac_f32_e32 v49, v50, v49
	v_mov_b32_e32 v50, s28
	v_div_scale_f32 v50, vcc, s32, v50, s32
	v_mul_f32_e32 v51, v50, v49
	v_fma_f32 v52, -v48, v51, v50
	v_fmac_f32_e32 v51, v52, v49
	v_fma_f32 v48, -v48, v51, v50
	v_div_fmas_f32 v48, v48, v49, v51
	v_div_fixup_f32 v48, v48, s28, v47
	v_cmp_gt_f32_e64 vcc, s28, 0
	v_writelane_b32 v40, s28, 7
	s_nop 0
	v_cndmask_b32_e32 v48, 0, v48, vcc
	v_fmaak_f32 v49, v18, v48, 0x4b400000
	v_fmaak_f32 v50, v19, v48, 0x4b400000
	v_fmaak_f32 v51, v20, v48, 0x4b400000
	v_fmaak_f32 v52, v21, v48, 0x4b400000
	v_perm_b32 v49, v50, v49, s33
	v_perm_b32 v51, v52, v51, s34
	v_or_b32_e32 v84, v49, v51
	v_fmaak_f32 v41, v22, v48, 0x4b400000
	v_fmaak_f32 v42, v23, v48, 0x4b400000
	v_fmaak_f32 v43, v24, v48, 0x4b400000
	v_fmaak_f32 v44, v25, v48, 0x4b400000
	v_perm_b32 v41, v42, v41, s33
	v_perm_b32 v43, v44, v43, s34
	v_or_b32_e32 v85, v41, v43
	v_fmaak_f32 v49, v26, v48, 0x4b400000
	v_fmaak_f32 v50, v27, v48, 0x4b400000
	v_fmaak_f32 v51, v28, v48, 0x4b400000
	v_fmaak_f32 v52, v29, v48, 0x4b400000
	v_perm_b32 v49, v50, v49, s33
	v_perm_b32 v51, v52, v51, s34
	v_or_b32_e32 v86, v49, v51
	v_fmaak_f32 v41, v30, v48, 0x4b400000
	v_fmaak_f32 v42, v31, v48, 0x4b400000
	v_fmaak_f32 v43, v32, v48, 0x4b400000
	v_fmaak_f32 v44, v33, v48, 0x4b400000
	v_perm_b32 v41, v42, v41, s33
	v_perm_b32 v43, v44, v43, s34
	v_or_b32_e32 v87, v41, v43
	s_waitcnt vmcnt(0)
	ds_read_b128 v[18:21], v38 offset:0
	ds_read_b128 v[22:25], v38 offset:1024
	ds_read_b128 v[26:29], v38 offset:2048
	ds_read_b128 v[30:33], v38 offset:3072
	s_waitcnt lgkmcnt(0)
	s_barrier
	s_mov_b32 m0, s36
	s_nop 0
	global_load_lds_dwordx4 v34, s[16:17] nt
	global_load_lds_dwordx4 v34, s[16:17] offset:1024 nt
	global_load_lds_dwordx4 v34, s[16:17] offset:2048 nt
	global_load_lds_dwordx4 v35, s[16:17] offset:3072 nt
	s_add_u32 s16, s16, 0x7d00
	s_addc_u32 s17, s17, 0
	v_cndmask_b32_e64 v30, 0, v30, s[18:19]
	v_cndmask_b32_e64 v31, 0, v31, s[18:19]
	v_cndmask_b32_e64 v32, 0, v32, s[18:19]
	v_cndmask_b32_e64 v33, 0, v33, s[18:19]
	v_max3_f32 v41, |v18|, |v19|, |v20|
	v_max3_f32 v42, |v21|, |v22|, |v23|
	v_max3_f32 v43, |v24|, |v25|, |v26|
	v_max3_f32 v44, |v27|, |v28|, |v29|
	v_max3_f32 v48, |v30|, |v31|, |v32|
	v_max3_f32 v41, v41, v42, |v33|
	v_max3_f32 v43, v43, v44, v48
	v_max_f32_e32 v41, v41, v43
	v_pk_add_f32 v[2:3], v[2:3], v[18:19]
	v_pk_add_f32 v[4:5], v[4:5], v[20:21]
	v_max_f32_dpp v41, v41, v41 quad_perm:[1,0,3,2] row_mask:0xf bank_mask:0xf
	v_pk_add_f32 v[6:7], v[6:7], v[22:23]
	v_pk_add_f32 v[8:9], v[8:9], v[24:25]
	v_max_f32_dpp v41, v41, v41 quad_perm:[2,3,0,1] row_mask:0xf bank_mask:0xf
	v_pk_add_f32 v[10:11], v[10:11], v[26:27]
	v_pk_add_f32 v[12:13], v[12:13], v[28:29]
	v_max_f32_dpp v41, v41, v41 row_half_mirror row_mask:0xf bank_mask:0xf
	v_pk_add_f32 v[14:15], v[14:15], v[30:31]
	v_pk_add_f32 v[16:17], v[16:17], v[32:33]
	v_max_f32_dpp v41, v41, v41 row_mirror row_mask:0xf bank_mask:0xf
	s_nop 1
	v_max_f32_dpp v41, v41, v41 row_bcast:15 row_mask:0xa bank_mask:0xf
	s_nop 1
	v_max_f32_dpp v41, v41, v41 row_bcast:31 row_mask:0xc bank_mask:0xf
	s_nop 1
	v_readlane_b32 s28, v41, 63
	s_nop 1
	v_div_scale_f32 v48, s[30:31], s28, s28, v47
	v_rcp_f32_e32 v49, v48
	s_nop 0
	v_fma_f32 v50, -v48, v49, 1.0
	v_fmac_f32_e32 v49, v50, v49
	v_mov_b32_e32 v50, s28
	v_div_scale_f32 v50, vcc, s32, v50, s32
	v_mul_f32_e32 v51, v50, v49
	v_fma_f32 v52, -v48, v51, v50
	v_fmac_f32_e32 v51, v52, v49
	v_fma_f32 v48, -v48, v51, v50
	v_div_fmas_f32 v48, v48, v49, v51
	v_div_fixup_f32 v48, v48, s28, v47
	v_cmp_gt_f32_e64 vcc, s28, 0
	v_writelane_b32 v40, s28, 8
	s_nop 0
	v_cndmask_b32_e32 v48, 0, v48, vcc
	v_fmaak_f32 v49, v18, v48, 0x4b400000
	v_fmaak_f32 v50, v19, v48, 0x4b400000
	v_fmaak_f32 v51, v20, v48, 0x4b400000
	v_fmaak_f32 v52, v21, v48, 0x4b400000
	v_perm_b32 v49, v50, v49, s33
	v_perm_b32 v51, v52, v51, s34
	v_or_b32_e32 v88, v49, v51
	v_fmaak_f32 v41, v22, v48, 0x4b400000
	v_fmaak_f32 v42, v23, v48, 0x4b400000
	v_fmaak_f32 v43, v24, v48, 0x4b400000
	v_fmaak_f32 v44, v25, v48, 0x4b400000
	v_perm_b32 v41, v42, v41, s33
	v_perm_b32 v43, v44, v43, s34
	v_or_b32_e32 v89, v41, v43
	v_fmaak_f32 v49, v26, v48, 0x4b400000
	v_fmaak_f32 v50, v27, v48, 0x4b400000
	v_fmaak_f32 v51, v28, v48, 0x4b400000
	v_fmaak_f32 v52, v29, v48, 0x4b400000
	v_perm_b32 v49, v50, v49, s33
	v_perm_b32 v51, v52, v51, s34
	v_or_b32_e32 v90, v49, v51
	v_fmaak_f32 v41, v30, v48, 0x4b400000
	v_fmaak_f32 v42, v31, v48, 0x4b400000
	v_fmaak_f32 v43, v32, v48, 0x4b400000
	v_fmaak_f32 v44, v33, v48, 0x4b400000
	v_perm_b32 v41, v42, v41, s33
	v_perm_b32 v43, v44, v43, s34
	v_or_b32_e32 v91, v41, v43
	s_waitcnt vmcnt(0)
	ds_read_b128 v[18:21], v38 offset:4096
	ds_read_b128 v[22:25], v38 offset:5120
	ds_read_b128 v[26:29], v38 offset:6144
	ds_read_b128 v[30:33], v38 offset:7168
	s_waitcnt lgkmcnt(0)
	s_barrier
	s_mov_b32 m0, s35
	s_nop 0
	global_load_lds_dwordx4 v34, s[16:17] nt
	global_load_lds_dwordx4 v34, s[16:17] offset:1024 nt
	global_load_lds_dwordx4 v34, s[16:17] offset:2048 nt
	global_load_lds_dwordx4 v35, s[16:17] offset:3072 nt
	s_add_u32 s16, s16, 0x7d00
	s_addc_u32 s17, s17, 0
	v_cndmask_b32_e64 v30, 0, v30, s[18:19]
	v_cndmask_b32_e64 v31, 0, v31, s[18:19]
	v_cndmask_b32_e64 v32, 0, v32, s[18:19]
	v_cndmask_b32_e64 v33, 0, v33, s[18:19]
	v_max3_f32 v41, |v18|, |v19|, |v20|
	v_max3_f32 v42, |v21|, |v22|, |v23|
	v_max3_f32 v43, |v24|, |v25|, |v26|
	v_max3_f32 v44, |v27|, |v28|, |v29|
	v_max3_f32 v48, |v30|, |v31|, |v32|
	v_max3_f32 v41, v41, v42, |v33|
	v_max3_f32 v43, v43, v44, v48
	v_max_f32_e32 v41, v41, v43
	v_pk_add_f32 v[2:3], v[2:3], v[18:19]
	v_pk_add_f32 v[4:5], v[4:5], v[20:21]
	v_max_f32_dpp v41, v41, v41 quad_perm:[1,0,3,2] row_mask:0xf bank_mask:0xf
	v_pk_add_f32 v[6:7], v[6:7], v[22:23]
	v_pk_add_f32 v[8:9], v[8:9], v[24:25]
	v_max_f32_dpp v41, v41, v41 quad_perm:[2,3,0,1] row_mask:0xf bank_mask:0xf
	v_pk_add_f32 v[10:11], v[10:11], v[26:27]
	v_pk_add_f32 v[12:13], v[12:13], v[28:29]
	v_max_f32_dpp v41, v41, v41 row_half_mirror row_mask:0xf bank_mask:0xf
	v_pk_add_f32 v[14:15], v[14:15], v[30:31]
	v_pk_add_f32 v[16:17], v[16:17], v[32:33]
	v_max_f32_dpp v41, v41, v41 row_mirror row_mask:0xf bank_mask:0xf
	s_nop 1
	v_max_f32_dpp v41, v41, v41 row_bcast:15 row_mask:0xa bank_mask:0xf
	s_nop 1
	v_max_f32_dpp v41, v41, v41 row_bcast:31 row_mask:0xc bank_mask:0xf
	s_nop 1
	v_readlane_b32 s28, v41, 63
	s_nop 1
	v_div_scale_f32 v48, s[30:31], s28, s28, v47
	v_rcp_f32_e32 v49, v48
	s_nop 0
	v_fma_f32 v50, -v48, v49, 1.0
	v_fmac_f32_e32 v49, v50, v49
	v_mov_b32_e32 v50, s28
	v_div_scale_f32 v50, vcc, s32, v50, s32
	v_mul_f32_e32 v51, v50, v49
	v_fma_f32 v52, -v48, v51, v50
	v_fmac_f32_e32 v51, v52, v49
	v_fma_f32 v48, -v48, v51, v50
	v_div_fmas_f32 v48, v48, v49, v51
	v_div_fixup_f32 v48, v48, s28, v47
	v_cmp_gt_f32_e64 vcc, s28, 0
	v_writelane_b32 v40, s28, 9
	s_nop 0
	v_cndmask_b32_e32 v48, 0, v48, vcc
	v_fmaak_f32 v49, v18, v48, 0x4b400000
	v_fmaak_f32 v50, v19, v48, 0x4b400000
	v_fmaak_f32 v51, v20, v48, 0x4b400000
	v_fmaak_f32 v52, v21, v48, 0x4b400000
	v_perm_b32 v49, v50, v49, s33
	v_perm_b32 v51, v52, v51, s34
	v_or_b32_e32 v92, v49, v51
	v_fmaak_f32 v41, v22, v48, 0x4b400000
	v_fmaak_f32 v42, v23, v48, 0x4b400000
	v_fmaak_f32 v43, v24, v48, 0x4b400000
	v_fmaak_f32 v44, v25, v48, 0x4b400000
	v_perm_b32 v41, v42, v41, s33
	v_perm_b32 v43, v44, v43, s34
	v_or_b32_e32 v93, v41, v43
	v_fmaak_f32 v49, v26, v48, 0x4b400000
	v_fmaak_f32 v50, v27, v48, 0x4b400000
	v_fmaak_f32 v51, v28, v48, 0x4b400000
	v_fmaak_f32 v52, v29, v48, 0x4b400000
	v_perm_b32 v49, v50, v49, s33
	v_perm_b32 v51, v52, v51, s34
	v_or_b32_e32 v94, v49, v51
	v_fmaak_f32 v41, v30, v48, 0x4b400000
	v_fmaak_f32 v42, v31, v48, 0x4b400000
	v_fmaak_f32 v43, v32, v48, 0x4b400000
	v_fmaak_f32 v44, v33, v48, 0x4b400000
	v_perm_b32 v41, v42, v41, s33
	v_perm_b32 v43, v44, v43, s34
	v_or_b32_e32 v95, v41, v43
	s_waitcnt vmcnt(0)
	ds_read_b128 v[18:21], v38 offset:0
	ds_read_b128 v[22:25], v38 offset:1024
	ds_read_b128 v[26:29], v38 offset:2048
	ds_read_b128 v[30:33], v38 offset:3072
	s_waitcnt lgkmcnt(0)
	s_barrier
	s_mov_b32 m0, s36
	s_nop 0
	global_load_lds_dwordx4 v34, s[16:17] nt
	global_load_lds_dwordx4 v34, s[16:17] offset:1024 nt
	global_load_lds_dwordx4 v34, s[16:17] offset:2048 nt
	global_load_lds_dwordx4 v35, s[16:17] offset:3072 nt
	s_add_u32 s16, s16, 0x7d00
	s_addc_u32 s17, s17, 0
	v_cndmask_b32_e64 v30, 0, v30, s[18:19]
	v_cndmask_b32_e64 v31, 0, v31, s[18:19]
	v_cndmask_b32_e64 v32, 0, v32, s[18:19]
	v_cndmask_b32_e64 v33, 0, v33, s[18:19]
	v_max3_f32 v41, |v18|, |v19|, |v20|
	v_max3_f32 v42, |v21|, |v22|, |v23|
	v_max3_f32 v43, |v24|, |v25|, |v26|
	v_max3_f32 v44, |v27|, |v28|, |v29|
	v_max3_f32 v48, |v30|, |v31|, |v32|
	v_max3_f32 v41, v41, v42, |v33|
	v_max3_f32 v43, v43, v44, v48
	v_max_f32_e32 v41, v41, v43
	v_pk_add_f32 v[2:3], v[2:3], v[18:19]
	v_pk_add_f32 v[4:5], v[4:5], v[20:21]
	v_max_f32_dpp v41, v41, v41 quad_perm:[1,0,3,2] row_mask:0xf bank_mask:0xf
	v_pk_add_f32 v[6:7], v[6:7], v[22:23]
	v_pk_add_f32 v[8:9], v[8:9], v[24:25]
	v_max_f32_dpp v41, v41, v41 quad_perm:[2,3,0,1] row_mask:0xf bank_mask:0xf
	v_pk_add_f32 v[10:11], v[10:11], v[26:27]
	v_pk_add_f32 v[12:13], v[12:13], v[28:29]
	v_max_f32_dpp v41, v41, v41 row_half_mirror row_mask:0xf bank_mask:0xf
	v_pk_add_f32 v[14:15], v[14:15], v[30:31]
	v_pk_add_f32 v[16:17], v[16:17], v[32:33]
	v_max_f32_dpp v41, v41, v41 row_mirror row_mask:0xf bank_mask:0xf
	s_nop 1
	v_max_f32_dpp v41, v41, v41 row_bcast:15 row_mask:0xa bank_mask:0xf
	s_nop 1
	v_max_f32_dpp v41, v41, v41 row_bcast:31 row_mask:0xc bank_mask:0xf
	s_nop 1
	v_readlane_b32 s28, v41, 63
	s_nop 1
	v_div_scale_f32 v48, s[30:31], s28, s28, v47
	v_rcp_f32_e32 v49, v48
	s_nop 0
	v_fma_f32 v50, -v48, v49, 1.0
	v_fmac_f32_e32 v49, v50, v49
	v_mov_b32_e32 v50, s28
	v_div_scale_f32 v50, vcc, s32, v50, s32
	v_mul_f32_e32 v51, v50, v49
	v_fma_f32 v52, -v48, v51, v50
	v_fmac_f32_e32 v51, v52, v49
	v_fma_f32 v48, -v48, v51, v50
	v_div_fmas_f32 v48, v48, v49, v51
	v_div_fixup_f32 v48, v48, s28, v47
	v_cmp_gt_f32_e64 vcc, s28, 0
	v_writelane_b32 v40, s28, 10
	s_nop 0
	v_cndmask_b32_e32 v48, 0, v48, vcc
	v_fmaak_f32 v49, v18, v48, 0x4b400000
	v_fmaak_f32 v50, v19, v48, 0x4b400000
	v_fmaak_f32 v51, v20, v48, 0x4b400000
	v_fmaak_f32 v52, v21, v48, 0x4b400000
	v_perm_b32 v49, v50, v49, s33
	v_perm_b32 v51, v52, v51, s34
	v_or_b32_e32 v96, v49, v51
	v_fmaak_f32 v41, v22, v48, 0x4b400000
	v_fmaak_f32 v42, v23, v48, 0x4b400000
	v_fmaak_f32 v43, v24, v48, 0x4b400000
	v_fmaak_f32 v44, v25, v48, 0x4b400000
	v_perm_b32 v41, v42, v41, s33
	v_perm_b32 v43, v44, v43, s34
	v_or_b32_e32 v97, v41, v43
	v_fmaak_f32 v49, v26, v48, 0x4b400000
	v_fmaak_f32 v50, v27, v48, 0x4b400000
	v_fmaak_f32 v51, v28, v48, 0x4b400000
	v_fmaak_f32 v52, v29, v48, 0x4b400000
	v_perm_b32 v49, v50, v49, s33
	v_perm_b32 v51, v52, v51, s34
	v_or_b32_e32 v98, v49, v51
	v_fmaak_f32 v41, v30, v48, 0x4b400000
	v_fmaak_f32 v42, v31, v48, 0x4b400000
	v_fmaak_f32 v43, v32, v48, 0x4b400000
	v_fmaak_f32 v44, v33, v48, 0x4b400000
	v_perm_b32 v41, v42, v41, s33
	v_perm_b32 v43, v44, v43, s34
	v_or_b32_e32 v99, v41, v43
	s_waitcnt vmcnt(0)
	ds_read_b128 v[18:21], v38 offset:4096
	ds_read_b128 v[22:25], v38 offset:5120
	ds_read_b128 v[26:29], v38 offset:6144
	ds_read_b128 v[30:33], v38 offset:7168
	s_waitcnt lgkmcnt(0)
	s_barrier
	s_mov_b32 m0, s35
	s_nop 0
	global_load_lds_dwordx4 v34, s[16:17] nt
	global_load_lds_dwordx4 v34, s[16:17] offset:1024 nt
	global_load_lds_dwordx4 v34, s[16:17] offset:2048 nt
	global_load_lds_dwordx4 v35, s[16:17] offset:3072 nt
	s_add_u32 s16, s16, 0x7d00
	s_addc_u32 s17, s17, 0
	v_cndmask_b32_e64 v30, 0, v30, s[18:19]
	v_cndmask_b32_e64 v31, 0, v31, s[18:19]
	v_cndmask_b32_e64 v32, 0, v32, s[18:19]
	v_cndmask_b32_e64 v33, 0, v33, s[18:19]
	v_max3_f32 v41, |v18|, |v19|, |v20|
	v_max3_f32 v42, |v21|, |v22|, |v23|
	v_max3_f32 v43, |v24|, |v25|, |v26|
	v_max3_f32 v44, |v27|, |v28|, |v29|
	v_max3_f32 v48, |v30|, |v31|, |v32|
	v_max3_f32 v41, v41, v42, |v33|
	v_max3_f32 v43, v43, v44, v48
	v_max_f32_e32 v41, v41, v43
	v_pk_add_f32 v[2:3], v[2:3], v[18:19]
	v_pk_add_f32 v[4:5], v[4:5], v[20:21]
	v_max_f32_dpp v41, v41, v41 quad_perm:[1,0,3,2] row_mask:0xf bank_mask:0xf
	v_pk_add_f32 v[6:7], v[6:7], v[22:23]
	v_pk_add_f32 v[8:9], v[8:9], v[24:25]
	v_max_f32_dpp v41, v41, v41 quad_perm:[2,3,0,1] row_mask:0xf bank_mask:0xf
	v_pk_add_f32 v[10:11], v[10:11], v[26:27]
	v_pk_add_f32 v[12:13], v[12:13], v[28:29]
	v_max_f32_dpp v41, v41, v41 row_half_mirror row_mask:0xf bank_mask:0xf
	v_pk_add_f32 v[14:15], v[14:15], v[30:31]
	v_pk_add_f32 v[16:17], v[16:17], v[32:33]
	v_max_f32_dpp v41, v41, v41 row_mirror row_mask:0xf bank_mask:0xf
	s_nop 1
	v_max_f32_dpp v41, v41, v41 row_bcast:15 row_mask:0xa bank_mask:0xf
	s_nop 1
	v_max_f32_dpp v41, v41, v41 row_bcast:31 row_mask:0xc bank_mask:0xf
	s_nop 1
	v_readlane_b32 s28, v41, 63
	s_nop 1
	v_div_scale_f32 v48, s[30:31], s28, s28, v47
	v_rcp_f32_e32 v49, v48
	s_nop 0
	v_fma_f32 v50, -v48, v49, 1.0
	v_fmac_f32_e32 v49, v50, v49
	v_mov_b32_e32 v50, s28
	v_div_scale_f32 v50, vcc, s32, v50, s32
	v_mul_f32_e32 v51, v50, v49
	v_fma_f32 v52, -v48, v51, v50
	v_fmac_f32_e32 v51, v52, v49
	v_fma_f32 v48, -v48, v51, v50
	v_div_fmas_f32 v48, v48, v49, v51
	v_div_fixup_f32 v48, v48, s28, v47
	v_cmp_gt_f32_e64 vcc, s28, 0
	v_writelane_b32 v40, s28, 11
	s_nop 0
	v_cndmask_b32_e32 v48, 0, v48, vcc
	v_fmaak_f32 v49, v18, v48, 0x4b400000
	v_fmaak_f32 v50, v19, v48, 0x4b400000
	v_fmaak_f32 v51, v20, v48, 0x4b400000
	v_fmaak_f32 v52, v21, v48, 0x4b400000
	v_perm_b32 v49, v50, v49, s33
	v_perm_b32 v51, v52, v51, s34
	v_or_b32_e32 v100, v49, v51
	v_fmaak_f32 v41, v22, v48, 0x4b400000
	v_fmaak_f32 v42, v23, v48, 0x4b400000
	v_fmaak_f32 v43, v24, v48, 0x4b400000
	v_fmaak_f32 v44, v25, v48, 0x4b400000
	v_perm_b32 v41, v42, v41, s33
	v_perm_b32 v43, v44, v43, s34
	v_or_b32_e32 v101, v41, v43
	v_fmaak_f32 v49, v26, v48, 0x4b400000
	v_fmaak_f32 v50, v27, v48, 0x4b400000
	v_fmaak_f32 v51, v28, v48, 0x4b400000
	v_fmaak_f32 v52, v29, v48, 0x4b400000
	v_perm_b32 v49, v50, v49, s33
	v_perm_b32 v51, v52, v51, s34
	v_or_b32_e32 v102, v49, v51
	v_fmaak_f32 v41, v30, v48, 0x4b400000
	v_fmaak_f32 v42, v31, v48, 0x4b400000
	v_fmaak_f32 v43, v32, v48, 0x4b400000
	v_fmaak_f32 v44, v33, v48, 0x4b400000
	v_perm_b32 v41, v42, v41, s33
	v_perm_b32 v43, v44, v43, s34
	v_or_b32_e32 v103, v41, v43
	s_waitcnt vmcnt(0)
	ds_read_b128 v[18:21], v38 offset:0
	ds_read_b128 v[22:25], v38 offset:1024
	ds_read_b128 v[26:29], v38 offset:2048
	ds_read_b128 v[30:33], v38 offset:3072
	s_waitcnt lgkmcnt(0)
	s_barrier
	s_mov_b32 m0, s36
	s_nop 0
	global_load_lds_dwordx4 v34, s[16:17] nt
	global_load_lds_dwordx4 v34, s[16:17] offset:1024 nt
	global_load_lds_dwordx4 v34, s[16:17] offset:2048 nt
	global_load_lds_dwordx4 v35, s[16:17] offset:3072 nt
	s_add_u32 s16, s16, 0x7d00
	s_addc_u32 s17, s17, 0
	v_cndmask_b32_e64 v30, 0, v30, s[18:19]
	v_cndmask_b32_e64 v31, 0, v31, s[18:19]
	v_cndmask_b32_e64 v32, 0, v32, s[18:19]
	v_cndmask_b32_e64 v33, 0, v33, s[18:19]
	v_max3_f32 v41, |v18|, |v19|, |v20|
	v_max3_f32 v42, |v21|, |v22|, |v23|
	v_max3_f32 v43, |v24|, |v25|, |v26|
	v_max3_f32 v44, |v27|, |v28|, |v29|
	v_max3_f32 v48, |v30|, |v31|, |v32|
	v_max3_f32 v41, v41, v42, |v33|
	v_max3_f32 v43, v43, v44, v48
	v_max_f32_e32 v41, v41, v43
	v_pk_add_f32 v[2:3], v[2:3], v[18:19]
	v_pk_add_f32 v[4:5], v[4:5], v[20:21]
	v_max_f32_dpp v41, v41, v41 quad_perm:[1,0,3,2] row_mask:0xf bank_mask:0xf
	v_pk_add_f32 v[6:7], v[6:7], v[22:23]
	v_pk_add_f32 v[8:9], v[8:9], v[24:25]
	v_max_f32_dpp v41, v41, v41 quad_perm:[2,3,0,1] row_mask:0xf bank_mask:0xf
	v_pk_add_f32 v[10:11], v[10:11], v[26:27]
	v_pk_add_f32 v[12:13], v[12:13], v[28:29]
	v_max_f32_dpp v41, v41, v41 row_half_mirror row_mask:0xf bank_mask:0xf
	v_pk_add_f32 v[14:15], v[14:15], v[30:31]
	v_pk_add_f32 v[16:17], v[16:17], v[32:33]
	v_max_f32_dpp v41, v41, v41 row_mirror row_mask:0xf bank_mask:0xf
	s_nop 1
	v_max_f32_dpp v41, v41, v41 row_bcast:15 row_mask:0xa bank_mask:0xf
	s_nop 1
	v_max_f32_dpp v41, v41, v41 row_bcast:31 row_mask:0xc bank_mask:0xf
	s_nop 1
	v_readlane_b32 s28, v41, 63
	s_nop 1
	v_div_scale_f32 v48, s[30:31], s28, s28, v47
	v_rcp_f32_e32 v49, v48
	s_nop 0
	v_fma_f32 v50, -v48, v49, 1.0
	v_fmac_f32_e32 v49, v50, v49
	v_mov_b32_e32 v50, s28
	v_div_scale_f32 v50, vcc, s32, v50, s32
	v_mul_f32_e32 v51, v50, v49
	v_fma_f32 v52, -v48, v51, v50
	v_fmac_f32_e32 v51, v52, v49
	v_fma_f32 v48, -v48, v51, v50
	v_div_fmas_f32 v48, v48, v49, v51
	v_div_fixup_f32 v48, v48, s28, v47
	v_cmp_gt_f32_e64 vcc, s28, 0
	v_writelane_b32 v40, s28, 12
	s_nop 0
	v_cndmask_b32_e32 v48, 0, v48, vcc
	v_fmaak_f32 v49, v18, v48, 0x4b400000
	v_fmaak_f32 v50, v19, v48, 0x4b400000
	v_fmaak_f32 v51, v20, v48, 0x4b400000
	v_fmaak_f32 v52, v21, v48, 0x4b400000
	v_perm_b32 v49, v50, v49, s33
	v_perm_b32 v51, v52, v51, s34
	v_or_b32_e32 v104, v49, v51
	v_fmaak_f32 v41, v22, v48, 0x4b400000
	v_fmaak_f32 v42, v23, v48, 0x4b400000
	v_fmaak_f32 v43, v24, v48, 0x4b400000
	v_fmaak_f32 v44, v25, v48, 0x4b400000
	v_perm_b32 v41, v42, v41, s33
	v_perm_b32 v43, v44, v43, s34
	v_or_b32_e32 v105, v41, v43
	v_fmaak_f32 v49, v26, v48, 0x4b400000
	v_fmaak_f32 v50, v27, v48, 0x4b400000
	v_fmaak_f32 v51, v28, v48, 0x4b400000
	v_fmaak_f32 v52, v29, v48, 0x4b400000
	v_perm_b32 v49, v50, v49, s33
	v_perm_b32 v51, v52, v51, s34
	v_or_b32_e32 v106, v49, v51
	v_fmaak_f32 v41, v30, v48, 0x4b400000
	v_fmaak_f32 v42, v31, v48, 0x4b400000
	v_fmaak_f32 v43, v32, v48, 0x4b400000
	v_fmaak_f32 v44, v33, v48, 0x4b400000
	v_perm_b32 v41, v42, v41, s33
	v_perm_b32 v43, v44, v43, s34
	v_or_b32_e32 v107, v41, v43
	s_waitcnt vmcnt(0)
	ds_read_b128 v[18:21], v38 offset:4096
	ds_read_b128 v[22:25], v38 offset:5120
	ds_read_b128 v[26:29], v38 offset:6144
	ds_read_b128 v[30:33], v38 offset:7168
	s_waitcnt lgkmcnt(0)
	s_barrier
	s_mov_b32 m0, s35
	s_nop 0
	global_load_lds_dwordx4 v34, s[16:17] nt
	global_load_lds_dwordx4 v34, s[16:17] offset:1024 nt
	global_load_lds_dwordx4 v34, s[16:17] offset:2048 nt
	global_load_lds_dwordx4 v35, s[16:17] offset:3072 nt
	s_add_u32 s16, s16, 0x7d00
	s_addc_u32 s17, s17, 0
	v_cndmask_b32_e64 v30, 0, v30, s[18:19]
	v_cndmask_b32_e64 v31, 0, v31, s[18:19]
	v_cndmask_b32_e64 v32, 0, v32, s[18:19]
	v_cndmask_b32_e64 v33, 0, v33, s[18:19]
	v_max3_f32 v41, |v18|, |v19|, |v20|
	v_max3_f32 v42, |v21|, |v22|, |v23|
	v_max3_f32 v43, |v24|, |v25|, |v26|
	v_max3_f32 v44, |v27|, |v28|, |v29|
	v_max3_f32 v48, |v30|, |v31|, |v32|
	v_max3_f32 v41, v41, v42, |v33|
	v_max3_f32 v43, v43, v44, v48
	v_max_f32_e32 v41, v41, v43
	v_pk_add_f32 v[2:3], v[2:3], v[18:19]
	v_pk_add_f32 v[4:5], v[4:5], v[20:21]
	v_max_f32_dpp v41, v41, v41 quad_perm:[1,0,3,2] row_mask:0xf bank_mask:0xf
	v_pk_add_f32 v[6:7], v[6:7], v[22:23]
	v_pk_add_f32 v[8:9], v[8:9], v[24:25]
	v_max_f32_dpp v41, v41, v41 quad_perm:[2,3,0,1] row_mask:0xf bank_mask:0xf
	v_pk_add_f32 v[10:11], v[10:11], v[26:27]
	v_pk_add_f32 v[12:13], v[12:13], v[28:29]
	v_max_f32_dpp v41, v41, v41 row_half_mirror row_mask:0xf bank_mask:0xf
	v_pk_add_f32 v[14:15], v[14:15], v[30:31]
	v_pk_add_f32 v[16:17], v[16:17], v[32:33]
	v_max_f32_dpp v41, v41, v41 row_mirror row_mask:0xf bank_mask:0xf
	s_nop 1
	v_max_f32_dpp v41, v41, v41 row_bcast:15 row_mask:0xa bank_mask:0xf
	s_nop 1
	v_max_f32_dpp v41, v41, v41 row_bcast:31 row_mask:0xc bank_mask:0xf
	s_nop 1
	v_readlane_b32 s28, v41, 63
	s_nop 1
	v_div_scale_f32 v48, s[30:31], s28, s28, v47
	v_rcp_f32_e32 v49, v48
	s_nop 0
	v_fma_f32 v50, -v48, v49, 1.0
	v_fmac_f32_e32 v49, v50, v49
	v_mov_b32_e32 v50, s28
	v_div_scale_f32 v50, vcc, s32, v50, s32
	v_mul_f32_e32 v51, v50, v49
	v_fma_f32 v52, -v48, v51, v50
	v_fmac_f32_e32 v51, v52, v49
	v_fma_f32 v48, -v48, v51, v50
	v_div_fmas_f32 v48, v48, v49, v51
	v_div_fixup_f32 v48, v48, s28, v47
	v_cmp_gt_f32_e64 vcc, s28, 0
	v_writelane_b32 v40, s28, 13
	s_nop 0
	v_cndmask_b32_e32 v48, 0, v48, vcc
	v_fmaak_f32 v49, v18, v48, 0x4b400000
	v_fmaak_f32 v50, v19, v48, 0x4b400000
	v_fmaak_f32 v51, v20, v48, 0x4b400000
	v_fmaak_f32 v52, v21, v48, 0x4b400000
	v_perm_b32 v49, v50, v49, s33
	v_perm_b32 v51, v52, v51, s34
	v_or_b32_e32 v108, v49, v51
	v_fmaak_f32 v41, v22, v48, 0x4b400000
	v_fmaak_f32 v42, v23, v48, 0x4b400000
	v_fmaak_f32 v43, v24, v48, 0x4b400000
	v_fmaak_f32 v44, v25, v48, 0x4b400000
	v_perm_b32 v41, v42, v41, s33
	v_perm_b32 v43, v44, v43, s34
	v_or_b32_e32 v109, v41, v43
	v_fmaak_f32 v49, v26, v48, 0x4b400000
	v_fmaak_f32 v50, v27, v48, 0x4b400000
	v_fmaak_f32 v51, v28, v48, 0x4b400000
	v_fmaak_f32 v52, v29, v48, 0x4b400000
	v_perm_b32 v49, v50, v49, s33
	v_perm_b32 v51, v52, v51, s34
	v_or_b32_e32 v110, v49, v51
	v_fmaak_f32 v41, v30, v48, 0x4b400000
	v_fmaak_f32 v42, v31, v48, 0x4b400000
	v_fmaak_f32 v43, v32, v48, 0x4b400000
	v_fmaak_f32 v44, v33, v48, 0x4b400000
	v_perm_b32 v41, v42, v41, s33
	v_perm_b32 v43, v44, v43, s34
	v_or_b32_e32 v111, v41, v43
	s_waitcnt vmcnt(0)
	ds_read_b128 v[18:21], v38 offset:0
	ds_read_b128 v[22:25], v38 offset:1024
	ds_read_b128 v[26:29], v38 offset:2048
	ds_read_b128 v[30:33], v38 offset:3072
	s_waitcnt lgkmcnt(0)
	s_barrier
	s_mov_b32 m0, s36
	s_nop 0
	global_load_lds_dwordx4 v34, s[16:17] nt
	global_load_lds_dwordx4 v34, s[16:17] offset:1024 nt
	global_load_lds_dwordx4 v34, s[16:17] offset:2048 nt
	global_load_lds_dwordx4 v35, s[16:17] offset:3072 nt
	s_add_u32 s16, s16, 0x7d00
	s_addc_u32 s17, s17, 0
	v_cndmask_b32_e64 v30, 0, v30, s[18:19]
	v_cndmask_b32_e64 v31, 0, v31, s[18:19]
	v_cndmask_b32_e64 v32, 0, v32, s[18:19]
	v_cndmask_b32_e64 v33, 0, v33, s[18:19]
	v_max3_f32 v41, |v18|, |v19|, |v20|
	v_max3_f32 v42, |v21|, |v22|, |v23|
	v_max3_f32 v43, |v24|, |v25|, |v26|
	v_max3_f32 v44, |v27|, |v28|, |v29|
	v_max3_f32 v48, |v30|, |v31|, |v32|
	v_max3_f32 v41, v41, v42, |v33|
	v_max3_f32 v43, v43, v44, v48
	v_max_f32_e32 v41, v41, v43
	v_pk_add_f32 v[2:3], v[2:3], v[18:19]
	v_pk_add_f32 v[4:5], v[4:5], v[20:21]
	v_max_f32_dpp v41, v41, v41 quad_perm:[1,0,3,2] row_mask:0xf bank_mask:0xf
	v_pk_add_f32 v[6:7], v[6:7], v[22:23]
	v_pk_add_f32 v[8:9], v[8:9], v[24:25]
	v_max_f32_dpp v41, v41, v41 quad_perm:[2,3,0,1] row_mask:0xf bank_mask:0xf
	v_pk_add_f32 v[10:11], v[10:11], v[26:27]
	v_pk_add_f32 v[12:13], v[12:13], v[28:29]
	v_max_f32_dpp v41, v41, v41 row_half_mirror row_mask:0xf bank_mask:0xf
	v_pk_add_f32 v[14:15], v[14:15], v[30:31]
	v_pk_add_f32 v[16:17], v[16:17], v[32:33]
	v_max_f32_dpp v41, v41, v41 row_mirror row_mask:0xf bank_mask:0xf
	s_nop 1
	v_max_f32_dpp v41, v41, v41 row_bcast:15 row_mask:0xa bank_mask:0xf
	s_nop 1
	v_max_f32_dpp v41, v41, v41 row_bcast:31 row_mask:0xc bank_mask:0xf
	s_nop 1
	v_readlane_b32 s28, v41, 63
	s_nop 1
	v_div_scale_f32 v48, s[30:31], s28, s28, v47
	v_rcp_f32_e32 v49, v48
	s_nop 0
	v_fma_f32 v50, -v48, v49, 1.0
	v_fmac_f32_e32 v49, v50, v49
	v_mov_b32_e32 v50, s28
	v_div_scale_f32 v50, vcc, s32, v50, s32
	v_mul_f32_e32 v51, v50, v49
	v_fma_f32 v52, -v48, v51, v50
	v_fmac_f32_e32 v51, v52, v49
	v_fma_f32 v48, -v48, v51, v50
	v_div_fmas_f32 v48, v48, v49, v51
	v_div_fixup_f32 v48, v48, s28, v47
	v_cmp_gt_f32_e64 vcc, s28, 0
	v_writelane_b32 v40, s28, 14
	s_nop 0
	v_cndmask_b32_e32 v48, 0, v48, vcc
	v_fmaak_f32 v49, v18, v48, 0x4b400000
	v_fmaak_f32 v50, v19, v48, 0x4b400000
	v_fmaak_f32 v51, v20, v48, 0x4b400000
	v_fmaak_f32 v52, v21, v48, 0x4b400000
	v_perm_b32 v49, v50, v49, s33
	v_perm_b32 v51, v52, v51, s34
	v_or_b32_e32 v112, v49, v51
	v_fmaak_f32 v41, v22, v48, 0x4b400000
	v_fmaak_f32 v42, v23, v48, 0x4b400000
	v_fmaak_f32 v43, v24, v48, 0x4b400000
	v_fmaak_f32 v44, v25, v48, 0x4b400000
	v_perm_b32 v41, v42, v41, s33
	v_perm_b32 v43, v44, v43, s34
	v_or_b32_e32 v113, v41, v43
	v_fmaak_f32 v49, v26, v48, 0x4b400000
	v_fmaak_f32 v50, v27, v48, 0x4b400000
	v_fmaak_f32 v51, v28, v48, 0x4b400000
	v_fmaak_f32 v52, v29, v48, 0x4b400000
	v_perm_b32 v49, v50, v49, s33
	v_perm_b32 v51, v52, v51, s34
	v_or_b32_e32 v114, v49, v51
	v_fmaak_f32 v41, v30, v48, 0x4b400000
	v_fmaak_f32 v42, v31, v48, 0x4b400000
	v_fmaak_f32 v43, v32, v48, 0x4b400000
	v_fmaak_f32 v44, v33, v48, 0x4b400000
	v_perm_b32 v41, v42, v41, s33
	v_perm_b32 v43, v44, v43, s34
	v_or_b32_e32 v115, v41, v43
	s_waitcnt vmcnt(0)
	ds_read_b128 v[18:21], v38 offset:4096
	ds_read_b128 v[22:25], v38 offset:5120
	ds_read_b128 v[26:29], v38 offset:6144
	ds_read_b128 v[30:33], v38 offset:7168
	s_waitcnt lgkmcnt(0)
	s_barrier
	s_mov_b32 m0, s35
	s_nop 0
	global_load_lds_dwordx4 v34, s[16:17] nt
	global_load_lds_dwordx4 v34, s[16:17] offset:1024 nt
	global_load_lds_dwordx4 v34, s[16:17] offset:2048 nt
	global_load_lds_dwordx4 v35, s[16:17] offset:3072 nt
	s_add_u32 s16, s16, 0x7d00
	s_addc_u32 s17, s17, 0
	v_cndmask_b32_e64 v30, 0, v30, s[18:19]
	v_cndmask_b32_e64 v31, 0, v31, s[18:19]
	v_cndmask_b32_e64 v32, 0, v32, s[18:19]
	v_cndmask_b32_e64 v33, 0, v33, s[18:19]
	v_max3_f32 v41, |v18|, |v19|, |v20|
	v_max3_f32 v42, |v21|, |v22|, |v23|
	v_max3_f32 v43, |v24|, |v25|, |v26|
	v_max3_f32 v44, |v27|, |v28|, |v29|
	v_max3_f32 v48, |v30|, |v31|, |v32|
	v_max3_f32 v41, v41, v42, |v33|
	v_max3_f32 v43, v43, v44, v48
	v_max_f32_e32 v41, v41, v43
	v_pk_add_f32 v[2:3], v[2:3], v[18:19]
	v_pk_add_f32 v[4:5], v[4:5], v[20:21]
	v_max_f32_dpp v41, v41, v41 quad_perm:[1,0,3,2] row_mask:0xf bank_mask:0xf
	v_pk_add_f32 v[6:7], v[6:7], v[22:23]
	v_pk_add_f32 v[8:9], v[8:9], v[24:25]
	v_max_f32_dpp v41, v41, v41 quad_perm:[2,3,0,1] row_mask:0xf bank_mask:0xf
	v_pk_add_f32 v[10:11], v[10:11], v[26:27]
	v_pk_add_f32 v[12:13], v[12:13], v[28:29]
	v_max_f32_dpp v41, v41, v41 row_half_mirror row_mask:0xf bank_mask:0xf
	v_pk_add_f32 v[14:15], v[14:15], v[30:31]
	v_pk_add_f32 v[16:17], v[16:17], v[32:33]
	v_max_f32_dpp v41, v41, v41 row_mirror row_mask:0xf bank_mask:0xf
	s_nop 1
	v_max_f32_dpp v41, v41, v41 row_bcast:15 row_mask:0xa bank_mask:0xf
	s_nop 1
	v_max_f32_dpp v41, v41, v41 row_bcast:31 row_mask:0xc bank_mask:0xf
	s_nop 1
	v_readlane_b32 s28, v41, 63
	s_nop 1
	v_div_scale_f32 v48, s[30:31], s28, s28, v47
	v_rcp_f32_e32 v49, v48
	s_nop 0
	v_fma_f32 v50, -v48, v49, 1.0
	v_fmac_f32_e32 v49, v50, v49
	v_mov_b32_e32 v50, s28
	v_div_scale_f32 v50, vcc, s32, v50, s32
	v_mul_f32_e32 v51, v50, v49
	v_fma_f32 v52, -v48, v51, v50
	v_fmac_f32_e32 v51, v52, v49
	v_fma_f32 v48, -v48, v51, v50
	v_div_fmas_f32 v48, v48, v49, v51
	v_div_fixup_f32 v48, v48, s28, v47
	v_cmp_gt_f32_e64 vcc, s28, 0
	v_writelane_b32 v40, s28, 15
	s_nop 0
	v_cndmask_b32_e32 v48, 0, v48, vcc
	v_fmaak_f32 v49, v18, v48, 0x4b400000
	v_fmaak_f32 v50, v19, v48, 0x4b400000
	v_fmaak_f32 v51, v20, v48, 0x4b400000
	v_fmaak_f32 v52, v21, v48, 0x4b400000
	v_perm_b32 v49, v50, v49, s33
	v_perm_b32 v51, v52, v51, s34
	v_or_b32_e32 v116, v49, v51
	v_fmaak_f32 v41, v22, v48, 0x4b400000
	v_fmaak_f32 v42, v23, v48, 0x4b400000
	v_fmaak_f32 v43, v24, v48, 0x4b400000
	v_fmaak_f32 v44, v25, v48, 0x4b400000
	v_perm_b32 v41, v42, v41, s33
	v_perm_b32 v43, v44, v43, s34
	v_or_b32_e32 v117, v41, v43
	v_fmaak_f32 v49, v26, v48, 0x4b400000
	v_fmaak_f32 v50, v27, v48, 0x4b400000
	v_fmaak_f32 v51, v28, v48, 0x4b400000
	v_fmaak_f32 v52, v29, v48, 0x4b400000
	v_perm_b32 v49, v50, v49, s33
	v_perm_b32 v51, v52, v51, s34
	v_or_b32_e32 v118, v49, v51
	v_fmaak_f32 v41, v30, v48, 0x4b400000
	v_fmaak_f32 v42, v31, v48, 0x4b400000
	v_fmaak_f32 v43, v32, v48, 0x4b400000
	v_fmaak_f32 v44, v33, v48, 0x4b400000
	v_perm_b32 v41, v42, v41, s33
	v_perm_b32 v43, v44, v43, s34
	v_or_b32_e32 v119, v41, v43
	s_waitcnt vmcnt(0)
	ds_read_b128 v[18:21], v38 offset:0
	ds_read_b128 v[22:25], v38 offset:1024
	ds_read_b128 v[26:29], v38 offset:2048
	ds_read_b128 v[30:33], v38 offset:3072
	s_waitcnt lgkmcnt(0)
	s_barrier
	s_mov_b32 m0, s36
	s_nop 0
	global_load_lds_dwordx4 v34, s[16:17] nt
	global_load_lds_dwordx4 v34, s[16:17] offset:1024 nt
	global_load_lds_dwordx4 v34, s[16:17] offset:2048 nt
	global_load_lds_dwordx4 v35, s[16:17] offset:3072 nt
	s_add_u32 s16, s16, 0x7d00
	s_addc_u32 s17, s17, 0
	v_cndmask_b32_e64 v30, 0, v30, s[18:19]
	v_cndmask_b32_e64 v31, 0, v31, s[18:19]
	v_cndmask_b32_e64 v32, 0, v32, s[18:19]
	v_cndmask_b32_e64 v33, 0, v33, s[18:19]
	v_max3_f32 v41, |v18|, |v19|, |v20|
	v_max3_f32 v42, |v21|, |v22|, |v23|
	v_max3_f32 v43, |v24|, |v25|, |v26|
	v_max3_f32 v44, |v27|, |v28|, |v29|
	v_max3_f32 v48, |v30|, |v31|, |v32|
	v_max3_f32 v41, v41, v42, |v33|
	v_max3_f32 v43, v43, v44, v48
	v_max_f32_e32 v41, v41, v43
	v_pk_add_f32 v[2:3], v[2:3], v[18:19]
	v_pk_add_f32 v[4:5], v[4:5], v[20:21]
	v_max_f32_dpp v41, v41, v41 quad_perm:[1,0,3,2] row_mask:0xf bank_mask:0xf
	v_pk_add_f32 v[6:7], v[6:7], v[22:23]
	v_pk_add_f32 v[8:9], v[8:9], v[24:25]
	v_max_f32_dpp v41, v41, v41 quad_perm:[2,3,0,1] row_mask:0xf bank_mask:0xf
	v_pk_add_f32 v[10:11], v[10:11], v[26:27]
	v_pk_add_f32 v[12:13], v[12:13], v[28:29]
	v_max_f32_dpp v41, v41, v41 row_half_mirror row_mask:0xf bank_mask:0xf
	v_pk_add_f32 v[14:15], v[14:15], v[30:31]
	v_pk_add_f32 v[16:17], v[16:17], v[32:33]
	v_max_f32_dpp v41, v41, v41 row_mirror row_mask:0xf bank_mask:0xf
	s_nop 1
	v_max_f32_dpp v41, v41, v41 row_bcast:15 row_mask:0xa bank_mask:0xf
	s_nop 1
	v_max_f32_dpp v41, v41, v41 row_bcast:31 row_mask:0xc bank_mask:0xf
	s_nop 1
	v_readlane_b32 s28, v41, 63
	s_nop 1
	v_div_scale_f32 v48, s[30:31], s28, s28, v47
	v_rcp_f32_e32 v49, v48
	s_nop 0
	v_fma_f32 v50, -v48, v49, 1.0
	v_fmac_f32_e32 v49, v50, v49
	v_mov_b32_e32 v50, s28
	v_div_scale_f32 v50, vcc, s32, v50, s32
	v_mul_f32_e32 v51, v50, v49
	v_fma_f32 v52, -v48, v51, v50
	v_fmac_f32_e32 v51, v52, v49
	v_fma_f32 v48, -v48, v51, v50
	v_div_fmas_f32 v48, v48, v49, v51
	v_div_fixup_f32 v48, v48, s28, v47
	v_cmp_gt_f32_e64 vcc, s28, 0
	v_writelane_b32 v40, s28, 16
	s_nop 0
	v_cndmask_b32_e32 v48, 0, v48, vcc
	v_fmaak_f32 v49, v18, v48, 0x4b400000
	v_fmaak_f32 v50, v19, v48, 0x4b400000
	v_fmaak_f32 v51, v20, v48, 0x4b400000
	v_fmaak_f32 v52, v21, v48, 0x4b400000
	v_perm_b32 v49, v50, v49, s33
	v_perm_b32 v51, v52, v51, s34
	v_or_b32_e32 v120, v49, v51
	v_fmaak_f32 v41, v22, v48, 0x4b400000
	v_fmaak_f32 v42, v23, v48, 0x4b400000
	v_fmaak_f32 v43, v24, v48, 0x4b400000
	v_fmaak_f32 v44, v25, v48, 0x4b400000
	v_perm_b32 v41, v42, v41, s33
	v_perm_b32 v43, v44, v43, s34
	v_or_b32_e32 v121, v41, v43
	v_fmaak_f32 v49, v26, v48, 0x4b400000
	v_fmaak_f32 v50, v27, v48, 0x4b400000
	v_fmaak_f32 v51, v28, v48, 0x4b400000
	v_fmaak_f32 v52, v29, v48, 0x4b400000
	v_perm_b32 v49, v50, v49, s33
	v_perm_b32 v51, v52, v51, s34
	v_or_b32_e32 v122, v49, v51
	v_fmaak_f32 v41, v30, v48, 0x4b400000
	v_fmaak_f32 v42, v31, v48, 0x4b400000
	v_fmaak_f32 v43, v32, v48, 0x4b400000
	v_fmaak_f32 v44, v33, v48, 0x4b400000
	v_perm_b32 v41, v42, v41, s33
	v_perm_b32 v43, v44, v43, s34
	v_or_b32_e32 v123, v41, v43
	s_waitcnt vmcnt(0)
	ds_read_b128 v[18:21], v38 offset:4096
	ds_read_b128 v[22:25], v38 offset:5120
	ds_read_b128 v[26:29], v38 offset:6144
	ds_read_b128 v[30:33], v38 offset:7168
	s_waitcnt lgkmcnt(0)
	s_barrier
	s_mov_b32 m0, s35
	s_nop 0
	global_load_lds_dwordx4 v34, s[16:17] nt
	global_load_lds_dwordx4 v34, s[16:17] offset:1024 nt
	global_load_lds_dwordx4 v34, s[16:17] offset:2048 nt
	global_load_lds_dwordx4 v35, s[16:17] offset:3072 nt
	s_add_u32 s16, s16, 0x7d00
	s_addc_u32 s17, s17, 0
	v_cndmask_b32_e64 v30, 0, v30, s[18:19]
	v_cndmask_b32_e64 v31, 0, v31, s[18:19]
	v_cndmask_b32_e64 v32, 0, v32, s[18:19]
	v_cndmask_b32_e64 v33, 0, v33, s[18:19]
	v_max3_f32 v41, |v18|, |v19|, |v20|
	v_max3_f32 v42, |v21|, |v22|, |v23|
	v_max3_f32 v43, |v24|, |v25|, |v26|
	v_max3_f32 v44, |v27|, |v28|, |v29|
	v_max3_f32 v48, |v30|, |v31|, |v32|
	v_max3_f32 v41, v41, v42, |v33|
	v_max3_f32 v43, v43, v44, v48
	v_max_f32_e32 v41, v41, v43
	v_pk_add_f32 v[2:3], v[2:3], v[18:19]
	v_pk_add_f32 v[4:5], v[4:5], v[20:21]
	v_max_f32_dpp v41, v41, v41 quad_perm:[1,0,3,2] row_mask:0xf bank_mask:0xf
	v_pk_add_f32 v[6:7], v[6:7], v[22:23]
	v_pk_add_f32 v[8:9], v[8:9], v[24:25]
	v_max_f32_dpp v41, v41, v41 quad_perm:[2,3,0,1] row_mask:0xf bank_mask:0xf
	v_pk_add_f32 v[10:11], v[10:11], v[26:27]
	v_pk_add_f32 v[12:13], v[12:13], v[28:29]
	v_max_f32_dpp v41, v41, v41 row_half_mirror row_mask:0xf bank_mask:0xf
	v_pk_add_f32 v[14:15], v[14:15], v[30:31]
	v_pk_add_f32 v[16:17], v[16:17], v[32:33]
	v_max_f32_dpp v41, v41, v41 row_mirror row_mask:0xf bank_mask:0xf
	s_nop 1
	v_max_f32_dpp v41, v41, v41 row_bcast:15 row_mask:0xa bank_mask:0xf
	s_nop 1
	v_max_f32_dpp v41, v41, v41 row_bcast:31 row_mask:0xc bank_mask:0xf
	s_nop 1
	v_readlane_b32 s28, v41, 63
	s_nop 1
	v_div_scale_f32 v48, s[30:31], s28, s28, v47
	v_rcp_f32_e32 v49, v48
	s_nop 0
	v_fma_f32 v50, -v48, v49, 1.0
	v_fmac_f32_e32 v49, v50, v49
	v_mov_b32_e32 v50, s28
	v_div_scale_f32 v50, vcc, s32, v50, s32
	v_mul_f32_e32 v51, v50, v49
	v_fma_f32 v52, -v48, v51, v50
	v_fmac_f32_e32 v51, v52, v49
	v_fma_f32 v48, -v48, v51, v50
	v_div_fmas_f32 v48, v48, v49, v51
	v_div_fixup_f32 v48, v48, s28, v47
	v_cmp_gt_f32_e64 vcc, s28, 0
	v_writelane_b32 v40, s28, 17
	s_nop 0
	v_cndmask_b32_e32 v48, 0, v48, vcc
	v_fmaak_f32 v49, v18, v48, 0x4b400000
	v_fmaak_f32 v50, v19, v48, 0x4b400000
	v_fmaak_f32 v51, v20, v48, 0x4b400000
	v_fmaak_f32 v52, v21, v48, 0x4b400000
	v_perm_b32 v49, v50, v49, s33
	v_perm_b32 v51, v52, v51, s34
	v_or_b32_e32 v124, v49, v51
	v_fmaak_f32 v41, v22, v48, 0x4b400000
	v_fmaak_f32 v42, v23, v48, 0x4b400000
	v_fmaak_f32 v43, v24, v48, 0x4b400000
	v_fmaak_f32 v44, v25, v48, 0x4b400000
	v_perm_b32 v41, v42, v41, s33
	v_perm_b32 v43, v44, v43, s34
	v_or_b32_e32 v125, v41, v43
	v_fmaak_f32 v49, v26, v48, 0x4b400000
	v_fmaak_f32 v50, v27, v48, 0x4b400000
	v_fmaak_f32 v51, v28, v48, 0x4b400000
	v_fmaak_f32 v52, v29, v48, 0x4b400000
	v_perm_b32 v49, v50, v49, s33
	v_perm_b32 v51, v52, v51, s34
	v_or_b32_e32 v126, v49, v51
	v_fmaak_f32 v41, v30, v48, 0x4b400000
	v_fmaak_f32 v42, v31, v48, 0x4b400000
	v_fmaak_f32 v43, v32, v48, 0x4b400000
	v_fmaak_f32 v44, v33, v48, 0x4b400000
	v_perm_b32 v41, v42, v41, s33
	v_perm_b32 v43, v44, v43, s34
	v_or_b32_e32 v127, v41, v43
	s_waitcnt vmcnt(0)
	ds_read_b128 v[18:21], v38 offset:0
	ds_read_b128 v[22:25], v38 offset:1024
	ds_read_b128 v[26:29], v38 offset:2048
	ds_read_b128 v[30:33], v38 offset:3072
	s_waitcnt lgkmcnt(0)
	s_barrier
	s_mov_b32 m0, s36
	s_nop 0
	global_load_lds_dwordx4 v34, s[16:17] nt
	global_load_lds_dwordx4 v34, s[16:17] offset:1024 nt
	global_load_lds_dwordx4 v34, s[16:17] offset:2048 nt
	global_load_lds_dwordx4 v35, s[16:17] offset:3072 nt
	s_add_u32 s16, s16, 0x7d00
	s_addc_u32 s17, s17, 0
	v_cndmask_b32_e64 v30, 0, v30, s[18:19]
	v_cndmask_b32_e64 v31, 0, v31, s[18:19]
	v_cndmask_b32_e64 v32, 0, v32, s[18:19]
	v_cndmask_b32_e64 v33, 0, v33, s[18:19]
	v_max3_f32 v41, |v18|, |v19|, |v20|
	v_max3_f32 v42, |v21|, |v22|, |v23|
	v_max3_f32 v43, |v24|, |v25|, |v26|
	v_max3_f32 v44, |v27|, |v28|, |v29|
	v_max3_f32 v48, |v30|, |v31|, |v32|
	v_max3_f32 v41, v41, v42, |v33|
	v_max3_f32 v43, v43, v44, v48
	v_max_f32_e32 v41, v41, v43
	v_pk_add_f32 v[2:3], v[2:3], v[18:19]
	v_pk_add_f32 v[4:5], v[4:5], v[20:21]
	v_max_f32_dpp v41, v41, v41 quad_perm:[1,0,3,2] row_mask:0xf bank_mask:0xf
	v_pk_add_f32 v[6:7], v[6:7], v[22:23]
	v_pk_add_f32 v[8:9], v[8:9], v[24:25]
	v_max_f32_dpp v41, v41, v41 quad_perm:[2,3,0,1] row_mask:0xf bank_mask:0xf
	v_pk_add_f32 v[10:11], v[10:11], v[26:27]
	v_pk_add_f32 v[12:13], v[12:13], v[28:29]
	v_max_f32_dpp v41, v41, v41 row_half_mirror row_mask:0xf bank_mask:0xf
	v_pk_add_f32 v[14:15], v[14:15], v[30:31]
	v_pk_add_f32 v[16:17], v[16:17], v[32:33]
	v_max_f32_dpp v41, v41, v41 row_mirror row_mask:0xf bank_mask:0xf
	s_nop 1
	v_max_f32_dpp v41, v41, v41 row_bcast:15 row_mask:0xa bank_mask:0xf
	s_nop 1
	v_max_f32_dpp v41, v41, v41 row_bcast:31 row_mask:0xc bank_mask:0xf
	s_nop 1
	v_readlane_b32 s28, v41, 63
	s_nop 1
	v_div_scale_f32 v48, s[30:31], s28, s28, v47
	v_rcp_f32_e32 v49, v48
	s_nop 0
	v_fma_f32 v50, -v48, v49, 1.0
	v_fmac_f32_e32 v49, v50, v49
	v_mov_b32_e32 v50, s28
	v_div_scale_f32 v50, vcc, s32, v50, s32
	v_mul_f32_e32 v51, v50, v49
	v_fma_f32 v52, -v48, v51, v50
	v_fmac_f32_e32 v51, v52, v49
	v_fma_f32 v48, -v48, v51, v50
	v_div_fmas_f32 v48, v48, v49, v51
	v_div_fixup_f32 v48, v48, s28, v47
	v_cmp_gt_f32_e64 vcc, s28, 0
	v_writelane_b32 v40, s28, 18
	s_nop 0
	v_cndmask_b32_e32 v48, 0, v48, vcc
	v_fmaak_f32 v49, v18, v48, 0x4b400000
	v_fmaak_f32 v50, v19, v48, 0x4b400000
	v_fmaak_f32 v51, v20, v48, 0x4b400000
	v_fmaak_f32 v52, v21, v48, 0x4b400000
	v_perm_b32 v49, v50, v49, s33
	v_perm_b32 v51, v52, v51, s34
	v_or_b32_e32 v36, v49, v51
	v_fmaak_f32 v41, v22, v48, 0x4b400000
	v_fmaak_f32 v42, v23, v48, 0x4b400000
	v_fmaak_f32 v43, v24, v48, 0x4b400000
	v_fmaak_f32 v44, v25, v48, 0x4b400000
	v_perm_b32 v41, v42, v41, s33
	v_perm_b32 v43, v44, v43, s34
	v_or_b32_e32 v37, v41, v43
	v_fmaak_f32 v49, v26, v48, 0x4b400000
	v_fmaak_f32 v50, v27, v48, 0x4b400000
	v_fmaak_f32 v51, v28, v48, 0x4b400000
	v_fmaak_f32 v52, v29, v48, 0x4b400000
	v_perm_b32 v49, v50, v49, s33
	v_perm_b32 v51, v52, v51, s34
	v_or_b32_e32 v45, v49, v51
	v_fmaak_f32 v41, v30, v48, 0x4b400000
	v_fmaak_f32 v42, v31, v48, 0x4b400000
	v_fmaak_f32 v43, v32, v48, 0x4b400000
	v_fmaak_f32 v44, v33, v48, 0x4b400000
	v_perm_b32 v41, v42, v41, s33
	v_perm_b32 v43, v44, v43, s34
	v_or_b32_e32 v46, v41, v43
	s_waitcnt vmcnt(0)
	ds_read_b128 v[18:21], v38 offset:4096
	ds_read_b128 v[22:25], v38 offset:5120
	ds_read_b128 v[26:29], v38 offset:6144
	ds_read_b128 v[30:33], v38 offset:7168
	s_waitcnt lgkmcnt(0)
	s_barrier
	s_mov_b32 m0, s35
	s_nop 0
	global_load_lds_dwordx4 v34, s[16:17] nt
	global_load_lds_dwordx4 v34, s[16:17] offset:1024 nt
	global_load_lds_dwordx4 v34, s[16:17] offset:2048 nt
	global_load_lds_dwordx4 v35, s[16:17] offset:3072 nt
	s_add_u32 s16, s16, 0x7d00
	s_addc_u32 s17, s17, 0
	v_cndmask_b32_e64 v30, 0, v30, s[18:19]
	v_cndmask_b32_e64 v31, 0, v31, s[18:19]
	v_cndmask_b32_e64 v32, 0, v32, s[18:19]
	v_cndmask_b32_e64 v33, 0, v33, s[18:19]
	v_max3_f32 v41, |v18|, |v19|, |v20|
	v_max3_f32 v42, |v21|, |v22|, |v23|
	v_max3_f32 v43, |v24|, |v25|, |v26|
	v_max3_f32 v44, |v27|, |v28|, |v29|
	v_max3_f32 v48, |v30|, |v31|, |v32|
	v_max3_f32 v41, v41, v42, |v33|
	v_max3_f32 v43, v43, v44, v48
	v_max_f32_e32 v41, v41, v43
	v_pk_add_f32 v[2:3], v[2:3], v[18:19]
	v_pk_add_f32 v[4:5], v[4:5], v[20:21]
	v_max_f32_dpp v41, v41, v41 quad_perm:[1,0,3,2] row_mask:0xf bank_mask:0xf
	v_pk_add_f32 v[6:7], v[6:7], v[22:23]
	v_pk_add_f32 v[8:9], v[8:9], v[24:25]
	v_max_f32_dpp v41, v41, v41 quad_perm:[2,3,0,1] row_mask:0xf bank_mask:0xf
	v_pk_add_f32 v[10:11], v[10:11], v[26:27]
	v_pk_add_f32 v[12:13], v[12:13], v[28:29]
	v_max_f32_dpp v41, v41, v41 row_half_mirror row_mask:0xf bank_mask:0xf
	v_pk_add_f32 v[14:15], v[14:15], v[30:31]
	v_pk_add_f32 v[16:17], v[16:17], v[32:33]
	v_max_f32_dpp v41, v41, v41 row_mirror row_mask:0xf bank_mask:0xf
	s_nop 1
	v_max_f32_dpp v41, v41, v41 row_bcast:15 row_mask:0xa bank_mask:0xf
	s_nop 1
	v_max_f32_dpp v41, v41, v41 row_bcast:31 row_mask:0xc bank_mask:0xf
	s_nop 1
	v_readlane_b32 s28, v41, 63
	s_nop 1
	v_div_scale_f32 v48, s[30:31], s28, s28, v47
	v_rcp_f32_e32 v49, v48
	s_nop 0
	v_fma_f32 v50, -v48, v49, 1.0
	v_fmac_f32_e32 v49, v50, v49
	v_mov_b32_e32 v50, s28
	v_div_scale_f32 v50, vcc, s32, v50, s32
	v_mul_f32_e32 v51, v50, v49
	v_fma_f32 v52, -v48, v51, v50
	v_fmac_f32_e32 v51, v52, v49
	v_fma_f32 v48, -v48, v51, v50
	v_div_fmas_f32 v48, v48, v49, v51
	v_div_fixup_f32 v48, v48, s28, v47
	v_cmp_gt_f32_e64 vcc, s28, 0
	v_writelane_b32 v40, s28, 19
	s_nop 0
	v_cndmask_b32_e32 v48, 0, v48, vcc
	v_fmaak_f32 v49, v18, v48, 0x4b400000
	v_fmaak_f32 v50, v19, v48, 0x4b400000
	v_fmaak_f32 v51, v20, v48, 0x4b400000
	v_fmaak_f32 v52, v21, v48, 0x4b400000
	v_perm_b32 v49, v50, v49, s33
	v_perm_b32 v51, v52, v51, s34
	v_or_b32_e32 v53, v49, v51
	v_fmaak_f32 v41, v22, v48, 0x4b400000
	v_fmaak_f32 v42, v23, v48, 0x4b400000
	v_fmaak_f32 v43, v24, v48, 0x4b400000
	v_fmaak_f32 v44, v25, v48, 0x4b400000
	v_perm_b32 v41, v42, v41, s33
	v_perm_b32 v43, v44, v43, s34
	v_or_b32_e32 v54, v41, v43
	v_fmaak_f32 v49, v26, v48, 0x4b400000
	v_fmaak_f32 v50, v27, v48, 0x4b400000
	v_fmaak_f32 v51, v28, v48, 0x4b400000
	v_fmaak_f32 v52, v29, v48, 0x4b400000
	v_perm_b32 v49, v50, v49, s33
	v_perm_b32 v51, v52, v51, s34
	v_or_b32_e32 v55, v49, v51
	v_fmaak_f32 v41, v30, v48, 0x4b400000
	v_fmaak_f32 v42, v31, v48, 0x4b400000
	v_fmaak_f32 v43, v32, v48, 0x4b400000
	v_fmaak_f32 v44, v33, v48, 0x4b400000
	v_perm_b32 v41, v42, v41, s33
	v_perm_b32 v43, v44, v43, s34
	v_or_b32_e32 v1, v41, v43
	s_waitcnt vmcnt(0)
	ds_read_b128 v[18:21], v38 offset:0
	ds_read_b128 v[22:25], v38 offset:1024
	ds_read_b128 v[26:29], v38 offset:2048
	ds_read_b128 v[30:33], v38 offset:3072
	s_waitcnt lgkmcnt(0)
	s_barrier
	s_mov_b32 m0, s36
	s_nop 0
	global_load_lds_dwordx4 v34, s[16:17] nt
	global_load_lds_dwordx4 v34, s[16:17] offset:1024 nt
	global_load_lds_dwordx4 v34, s[16:17] offset:2048 nt
	global_load_lds_dwordx4 v35, s[16:17] offset:3072 nt
	s_add_u32 s16, s16, 0x7d00
	s_addc_u32 s17, s17, 0
	v_cndmask_b32_e64 v30, 0, v30, s[18:19]
	v_cndmask_b32_e64 v31, 0, v31, s[18:19]
	v_cndmask_b32_e64 v32, 0, v32, s[18:19]
	v_cndmask_b32_e64 v33, 0, v33, s[18:19]
	v_max3_f32 v41, |v18|, |v19|, |v20|
	v_max3_f32 v42, |v21|, |v22|, |v23|
	v_max3_f32 v43, |v24|, |v25|, |v26|
	v_max3_f32 v44, |v27|, |v28|, |v29|
	v_max3_f32 v48, |v30|, |v31|, |v32|
	v_max3_f32 v41, v41, v42, |v33|
	v_max3_f32 v43, v43, v44, v48
	v_max_f32_e32 v41, v41, v43
	v_pk_add_f32 v[2:3], v[2:3], v[18:19]
	v_pk_add_f32 v[4:5], v[4:5], v[20:21]
	v_max_f32_dpp v41, v41, v41 quad_perm:[1,0,3,2] row_mask:0xf bank_mask:0xf
	v_pk_add_f32 v[6:7], v[6:7], v[22:23]
	v_pk_add_f32 v[8:9], v[8:9], v[24:25]
	v_max_f32_dpp v41, v41, v41 quad_perm:[2,3,0,1] row_mask:0xf bank_mask:0xf
	v_pk_add_f32 v[10:11], v[10:11], v[26:27]
	v_pk_add_f32 v[12:13], v[12:13], v[28:29]
	v_max_f32_dpp v41, v41, v41 row_half_mirror row_mask:0xf bank_mask:0xf
	v_pk_add_f32 v[14:15], v[14:15], v[30:31]
	v_pk_add_f32 v[16:17], v[16:17], v[32:33]
	v_max_f32_dpp v41, v41, v41 row_mirror row_mask:0xf bank_mask:0xf
	s_nop 1
	v_max_f32_dpp v41, v41, v41 row_bcast:15 row_mask:0xa bank_mask:0xf
	s_nop 1
	v_max_f32_dpp v41, v41, v41 row_bcast:31 row_mask:0xc bank_mask:0xf
	s_nop 1
	v_readlane_b32 s28, v41, 63
	s_nop 1
	v_div_scale_f32 v48, s[30:31], s28, s28, v47
	v_rcp_f32_e32 v49, v48
	s_nop 0
	v_fma_f32 v50, -v48, v49, 1.0
	v_fmac_f32_e32 v49, v50, v49
	v_mov_b32_e32 v50, s28
	v_div_scale_f32 v50, vcc, s32, v50, s32
	v_mul_f32_e32 v51, v50, v49
	v_fma_f32 v52, -v48, v51, v50
	v_fmac_f32_e32 v51, v52, v49
	v_fma_f32 v48, -v48, v51, v50
	v_div_fmas_f32 v48, v48, v49, v51
	v_div_fixup_f32 v48, v48, s28, v47
	v_cmp_gt_f32_e64 vcc, s28, 0
	v_writelane_b32 v40, s28, 20
	s_nop 0
	v_cndmask_b32_e32 v48, 0, v48, vcc
	v_fmaak_f32 v49, v18, v48, 0x4b400000
	v_fmaak_f32 v50, v19, v48, 0x4b400000
	v_fmaak_f32 v51, v20, v48, 0x4b400000
	v_fmaak_f32 v52, v21, v48, 0x4b400000
	v_perm_b32 v49, v50, v49, s33
	v_perm_b32 v51, v52, v51, s34
	v_or_b32_e32 v49, v49, v51
	s_add_u32 s20, s20, 0x5000
	s_addc_u32 s21, s21, 0
	s_add_u32 s22, s22, 0x5000
	s_addc_u32 s23, s23, 0
	s_add_u32 s24, s24, 0x5000
	s_addc_u32 s25, s25, 0
	s_add_u32 s26, s26, 0x5000
	s_addc_u32 s27, s27, 0
	global_store_dword v39, v49, s[20:21]
	v_fmaak_f32 v41, v22, v48, 0x4b400000
	v_fmaak_f32 v42, v23, v48, 0x4b400000
	v_fmaak_f32 v43, v24, v48, 0x4b400000
	v_fmaak_f32 v44, v25, v48, 0x4b400000
	v_perm_b32 v41, v42, v41, s33
	v_perm_b32 v43, v44, v43, s34
	v_or_b32_e32 v41, v41, v43
	global_store_dword v39, v41, s[22:23]
	v_fmaak_f32 v49, v26, v48, 0x4b400000
	v_fmaak_f32 v50, v27, v48, 0x4b400000
	v_fmaak_f32 v51, v28, v48, 0x4b400000
	v_fmaak_f32 v52, v29, v48, 0x4b400000
	v_perm_b32 v49, v50, v49, s33
	v_perm_b32 v51, v52, v51, s34
	v_or_b32_e32 v49, v49, v51
	global_store_dword v39, v49, s[24:25]
	v_fmaak_f32 v41, v30, v48, 0x4b400000
	v_fmaak_f32 v42, v31, v48, 0x4b400000
	v_fmaak_f32 v43, v32, v48, 0x4b400000
	v_fmaak_f32 v44, v33, v48, 0x4b400000
	v_perm_b32 v41, v42, v41, s33
	v_perm_b32 v43, v44, v43, s34
	v_or_b32_e32 v41, v41, v43
	global_store_dword v39, v41, s[26:27]
	s_waitcnt vmcnt(4)
	ds_read_b128 v[18:21], v38 offset:4096
	ds_read_b128 v[22:25], v38 offset:5120
	ds_read_b128 v[26:29], v38 offset:6144
	ds_read_b128 v[30:33], v38 offset:7168
	s_waitcnt lgkmcnt(0)
	s_barrier
	s_mov_b32 m0, s35
	s_nop 0
	global_load_lds_dwordx4 v34, s[16:17] nt
	global_load_lds_dwordx4 v34, s[16:17] offset:1024 nt
	global_load_lds_dwordx4 v34, s[16:17] offset:2048 nt
	global_load_lds_dwordx4 v35, s[16:17] offset:3072 nt
	s_add_u32 s16, s16, 0x7d00
	s_addc_u32 s17, s17, 0
	v_cndmask_b32_e64 v30, 0, v30, s[18:19]
	v_cndmask_b32_e64 v31, 0, v31, s[18:19]
	v_cndmask_b32_e64 v32, 0, v32, s[18:19]
	v_cndmask_b32_e64 v33, 0, v33, s[18:19]
	v_max3_f32 v41, |v18|, |v19|, |v20|
	v_max3_f32 v42, |v21|, |v22|, |v23|
	v_max3_f32 v43, |v24|, |v25|, |v26|
	v_max3_f32 v44, |v27|, |v28|, |v29|
	v_max3_f32 v48, |v30|, |v31|, |v32|
	v_max3_f32 v41, v41, v42, |v33|
	v_max3_f32 v43, v43, v44, v48
	v_max_f32_e32 v41, v41, v43
	v_pk_add_f32 v[2:3], v[2:3], v[18:19]
	v_pk_add_f32 v[4:5], v[4:5], v[20:21]
	v_max_f32_dpp v41, v41, v41 quad_perm:[1,0,3,2] row_mask:0xf bank_mask:0xf
	v_pk_add_f32 v[6:7], v[6:7], v[22:23]
	v_pk_add_f32 v[8:9], v[8:9], v[24:25]
	v_max_f32_dpp v41, v41, v41 quad_perm:[2,3,0,1] row_mask:0xf bank_mask:0xf
	v_pk_add_f32 v[10:11], v[10:11], v[26:27]
	v_pk_add_f32 v[12:13], v[12:13], v[28:29]
	v_max_f32_dpp v41, v41, v41 row_half_mirror row_mask:0xf bank_mask:0xf
	v_pk_add_f32 v[14:15], v[14:15], v[30:31]
	v_pk_add_f32 v[16:17], v[16:17], v[32:33]
	v_max_f32_dpp v41, v41, v41 row_mirror row_mask:0xf bank_mask:0xf
	s_nop 1
	v_max_f32_dpp v41, v41, v41 row_bcast:15 row_mask:0xa bank_mask:0xf
	s_nop 1
	v_max_f32_dpp v41, v41, v41 row_bcast:31 row_mask:0xc bank_mask:0xf
	s_nop 1
	v_readlane_b32 s28, v41, 63
	s_nop 1
	v_div_scale_f32 v48, s[30:31], s28, s28, v47
	v_rcp_f32_e32 v49, v48
	s_nop 0
	v_fma_f32 v50, -v48, v49, 1.0
	v_fmac_f32_e32 v49, v50, v49
	v_mov_b32_e32 v50, s28
	v_div_scale_f32 v50, vcc, s32, v50, s32
	v_mul_f32_e32 v51, v50, v49
	v_fma_f32 v52, -v48, v51, v50
	v_fmac_f32_e32 v51, v52, v49
	v_fma_f32 v48, -v48, v51, v50
	v_div_fmas_f32 v48, v48, v49, v51
	v_div_fixup_f32 v48, v48, s28, v47
	v_cmp_gt_f32_e64 vcc, s28, 0
	v_writelane_b32 v40, s28, 21
	s_nop 0
	v_cndmask_b32_e32 v48, 0, v48, vcc
	v_fmaak_f32 v49, v18, v48, 0x4b400000
	v_fmaak_f32 v50, v19, v48, 0x4b400000
	v_fmaak_f32 v51, v20, v48, 0x4b400000
	v_fmaak_f32 v52, v21, v48, 0x4b400000
	v_perm_b32 v49, v50, v49, s33
	v_perm_b32 v51, v52, v51, s34
	v_or_b32_e32 v49, v49, v51
	s_add_u32 s20, s20, 0x400
	s_addc_u32 s21, s21, 0
	s_add_u32 s22, s22, 0x400
	s_addc_u32 s23, s23, 0
	s_add_u32 s24, s24, 0x400
	s_addc_u32 s25, s25, 0
	s_add_u32 s26, s26, 0x400
	s_addc_u32 s27, s27, 0
	global_store_dword v39, v49, s[20:21]
	v_fmaak_f32 v41, v22, v48, 0x4b400000
	v_fmaak_f32 v42, v23, v48, 0x4b400000
	v_fmaak_f32 v43, v24, v48, 0x4b400000
	v_fmaak_f32 v44, v25, v48, 0x4b400000
	v_perm_b32 v41, v42, v41, s33
	v_perm_b32 v43, v44, v43, s34
	v_or_b32_e32 v41, v41, v43
	global_store_dword v39, v41, s[22:23]
	v_fmaak_f32 v49, v26, v48, 0x4b400000
	v_fmaak_f32 v50, v27, v48, 0x4b400000
	v_fmaak_f32 v51, v28, v48, 0x4b400000
	v_fmaak_f32 v52, v29, v48, 0x4b400000
	v_perm_b32 v49, v50, v49, s33
	v_perm_b32 v51, v52, v51, s34
	v_or_b32_e32 v49, v49, v51
	global_store_dword v39, v49, s[24:25]
	v_fmaak_f32 v41, v30, v48, 0x4b400000
	v_fmaak_f32 v42, v31, v48, 0x4b400000
	v_fmaak_f32 v43, v32, v48, 0x4b400000
	v_fmaak_f32 v44, v33, v48, 0x4b400000
	v_perm_b32 v41, v42, v41, s33
	v_perm_b32 v43, v44, v43, s34
	v_or_b32_e32 v41, v41, v43
	global_store_dword v39, v41, s[26:27]
	s_waitcnt vmcnt(4)
	ds_read_b128 v[18:21], v38 offset:0
	ds_read_b128 v[22:25], v38 offset:1024
	ds_read_b128 v[26:29], v38 offset:2048
	ds_read_b128 v[30:33], v38 offset:3072
	s_waitcnt lgkmcnt(0)
	s_barrier
	s_mov_b32 m0, s36
	s_nop 0
	global_load_lds_dwordx4 v34, s[16:17] nt
	global_load_lds_dwordx4 v34, s[16:17] offset:1024 nt
	global_load_lds_dwordx4 v34, s[16:17] offset:2048 nt
	global_load_lds_dwordx4 v35, s[16:17] offset:3072 nt
	s_add_u32 s16, s16, 0x7d00
	s_addc_u32 s17, s17, 0
	v_cndmask_b32_e64 v30, 0, v30, s[18:19]
	v_cndmask_b32_e64 v31, 0, v31, s[18:19]
	v_cndmask_b32_e64 v32, 0, v32, s[18:19]
	v_cndmask_b32_e64 v33, 0, v33, s[18:19]
	v_max3_f32 v41, |v18|, |v19|, |v20|
	v_max3_f32 v42, |v21|, |v22|, |v23|
	v_max3_f32 v43, |v24|, |v25|, |v26|
	v_max3_f32 v44, |v27|, |v28|, |v29|
	v_max3_f32 v48, |v30|, |v31|, |v32|
	v_max3_f32 v41, v41, v42, |v33|
	v_max3_f32 v43, v43, v44, v48
	v_max_f32_e32 v41, v41, v43
	v_pk_add_f32 v[2:3], v[2:3], v[18:19]
	v_pk_add_f32 v[4:5], v[4:5], v[20:21]
	v_max_f32_dpp v41, v41, v41 quad_perm:[1,0,3,2] row_mask:0xf bank_mask:0xf
	v_pk_add_f32 v[6:7], v[6:7], v[22:23]
	v_pk_add_f32 v[8:9], v[8:9], v[24:25]
	v_max_f32_dpp v41, v41, v41 quad_perm:[2,3,0,1] row_mask:0xf bank_mask:0xf
	v_pk_add_f32 v[10:11], v[10:11], v[26:27]
	v_pk_add_f32 v[12:13], v[12:13], v[28:29]
	v_max_f32_dpp v41, v41, v41 row_half_mirror row_mask:0xf bank_mask:0xf
	v_pk_add_f32 v[14:15], v[14:15], v[30:31]
	v_pk_add_f32 v[16:17], v[16:17], v[32:33]
	v_max_f32_dpp v41, v41, v41 row_mirror row_mask:0xf bank_mask:0xf
	s_nop 1
	v_max_f32_dpp v41, v41, v41 row_bcast:15 row_mask:0xa bank_mask:0xf
	s_nop 1
	v_max_f32_dpp v41, v41, v41 row_bcast:31 row_mask:0xc bank_mask:0xf
	s_nop 1
	v_readlane_b32 s28, v41, 63
	s_nop 1
	v_div_scale_f32 v48, s[30:31], s28, s28, v47
	v_rcp_f32_e32 v49, v48
	s_nop 0
	v_fma_f32 v50, -v48, v49, 1.0
	v_fmac_f32_e32 v49, v50, v49
	v_mov_b32_e32 v50, s28
	v_div_scale_f32 v50, vcc, s32, v50, s32
	v_mul_f32_e32 v51, v50, v49
	v_fma_f32 v52, -v48, v51, v50
	v_fmac_f32_e32 v51, v52, v49
	v_fma_f32 v48, -v48, v51, v50
	v_div_fmas_f32 v48, v48, v49, v51
	v_div_fixup_f32 v48, v48, s28, v47
	v_cmp_gt_f32_e64 vcc, s28, 0
	v_writelane_b32 v40, s28, 22
	s_nop 0
	v_cndmask_b32_e32 v48, 0, v48, vcc
	v_fmaak_f32 v49, v18, v48, 0x4b400000
	v_fmaak_f32 v50, v19, v48, 0x4b400000
	v_fmaak_f32 v51, v20, v48, 0x4b400000
	v_fmaak_f32 v52, v21, v48, 0x4b400000
	v_perm_b32 v49, v50, v49, s33
	v_perm_b32 v51, v52, v51, s34
	v_or_b32_e32 v49, v49, v51
	s_add_u32 s20, s20, 0x400
	s_addc_u32 s21, s21, 0
	s_add_u32 s22, s22, 0x400
	s_addc_u32 s23, s23, 0
	s_add_u32 s24, s24, 0x400
	s_addc_u32 s25, s25, 0
	s_add_u32 s26, s26, 0x400
	s_addc_u32 s27, s27, 0
	global_store_dword v39, v49, s[20:21]
	v_fmaak_f32 v41, v22, v48, 0x4b400000
	v_fmaak_f32 v42, v23, v48, 0x4b400000
	v_fmaak_f32 v43, v24, v48, 0x4b400000
	v_fmaak_f32 v44, v25, v48, 0x4b400000
	v_perm_b32 v41, v42, v41, s33
	v_perm_b32 v43, v44, v43, s34
	v_or_b32_e32 v41, v41, v43
	global_store_dword v39, v41, s[22:23]
	v_fmaak_f32 v49, v26, v48, 0x4b400000
	v_fmaak_f32 v50, v27, v48, 0x4b400000
	v_fmaak_f32 v51, v28, v48, 0x4b400000
	v_fmaak_f32 v52, v29, v48, 0x4b400000
	v_perm_b32 v49, v50, v49, s33
	v_perm_b32 v51, v52, v51, s34
	v_or_b32_e32 v49, v49, v51
	global_store_dword v39, v49, s[24:25]
	v_fmaak_f32 v41, v30, v48, 0x4b400000
	v_fmaak_f32 v42, v31, v48, 0x4b400000
	v_fmaak_f32 v43, v32, v48, 0x4b400000
	v_fmaak_f32 v44, v33, v48, 0x4b400000
	v_perm_b32 v41, v42, v41, s33
	v_perm_b32 v43, v44, v43, s34
	v_or_b32_e32 v41, v41, v43
	global_store_dword v39, v41, s[26:27]
	s_waitcnt vmcnt(4)
	ds_read_b128 v[18:21], v38 offset:4096
	ds_read_b128 v[22:25], v38 offset:5120
	ds_read_b128 v[26:29], v38 offset:6144
	ds_read_b128 v[30:33], v38 offset:7168
	s_waitcnt lgkmcnt(0)
	s_cmp_eq_u32 s29, 1
	s_cbranch_scc0 .Lk1_nodma24
	s_mov_b32 m0, s35
	s_nop 0
	global_load_lds_dwordx4 v34, s[16:17] nt
	global_load_lds_dwordx4 v34, s[16:17] offset:1024 nt
	global_load_lds_dwordx4 v34, s[16:17] offset:2048 nt
	global_load_lds_dwordx4 v35, s[16:17] offset:3072 nt
	s_add_u32 s16, s16, 0x7d00
	s_addc_u32 s17, s17, 0
